# GEMM epilogue stores write-through (sc1) so the grid barriers' L2 write-back has little to flush
# baseline (speedup 1.0000x reference)
.LBB0_382:
	s_and_b32 s22, s56, 0x7ffffffc
	s_cmp_eq_u32 s22, 24
	s_cselect_b64 vcc, -1, 0
	s_cmp_lg_u32 s22, 12
	v_cndmask_b32_e32 v1, 1.0, v163, vcc
	s_cselect_b64 vcc, -1, 0
	s_cmp_gt_i32 s56, 3
	v_cndmask_b32_e32 v1, v164, v1, vcc
	s_cselect_b64 vcc, -1, 0
	v_lshl_or_b32 v146, s56, 8, v157
	v_cndmask_b32_e32 v142, v165, v1, vcc
	v_lshl_add_u32 v1, s55, 8, v156
	v_ashrrev_i32_e32 v147, 31, v146
	v_mov_b64_e32 v[144:145], s[88:89]
	v_mad_i64_i32 v[166:167], s[22:23], v1, s48, v[144:145]
	v_lshlrev_b64 v[146:147], 1, v[146:147]
	v_lshl_add_u64 v[166:167], v[166:167], 0, v[146:147]
	v_pk_mul_f32 v[128:129], v[142:143], v[128:129] op_sel_hi:[0,1]
	v_pk_mul_f32 v[126:127], v[142:143], v[126:127] op_sel_hi:[0,1]
	v_pk_mul_f32 v[168:169], v[142:143], v[124:125] op_sel_hi:[0,1]
	v_pk_mul_f32 v[124:125], v[142:143], v[122:123] op_sel_hi:[0,1]
	v_cvt_pk_bf16_f32 v122, v126, v127
	v_cvt_pk_bf16_f32 v123, v128, v129
	v_cvt_pk_bf16_f32 v124, v124, v125
	v_cvt_pk_bf16_f32 v125, v168, v169
	global_store_dwordx4 v[166:167], v[122:125], off sc1
	v_pk_mul_f32 v[118:119], v[142:143], v[118:119] op_sel_hi:[0,1]
	v_pk_mul_f32 v[120:121], v[142:143], v[120:121] op_sel_hi:[0,1]
	v_pk_mul_f32 v[122:123], v[142:143], v[112:113] op_sel_hi:[0,1]
	v_pk_mul_f32 v[112:113], v[142:143], v[110:111] op_sel_hi:[0,1]
	v_cvt_pk_bf16_f32 v110, v118, v119
	v_cvt_pk_bf16_f32 v111, v120, v121
	v_cvt_pk_bf16_f32 v112, v112, v113
	v_cvt_pk_bf16_f32 v113, v122, v123
	global_store_dwordx4 v[166:167], v[110:113], off offset:256 sc1
	v_pk_mul_f32 v[114:115], v[142:143], v[114:115] op_sel_hi:[0,1]
	v_pk_mul_f32 v[102:103], v[142:143], v[102:103] op_sel_hi:[0,1]
	v_or_b32_e32 v110, 16, v1
	v_mad_i64_i32 v[110:111], s[22:23], v110, s48, v[144:145]
	v_lshl_add_u64 v[110:111], v[110:111], 0, v[146:147]
	v_pk_mul_f32 v[112:113], v[142:143], v[116:117] op_sel_hi:[0,1]
	v_pk_mul_f32 v[116:117], v[142:143], v[108:109] op_sel_hi:[0,1]
	v_pk_mul_f32 v[108:109], v[142:143], v[106:107] op_sel_hi:[0,1]
	v_cvt_pk_bf16_f32 v106, v114, v115
	v_cvt_pk_bf16_f32 v107, v112, v113
	v_cvt_pk_bf16_f32 v108, v108, v109
	v_cvt_pk_bf16_f32 v109, v116, v117
	global_store_dwordx4 v[110:111], v[106:109], off sc1
	v_pk_mul_f32 v[104:105], v[142:143], v[104:105] op_sel_hi:[0,1]
	v_pk_mul_f32 v[98:99], v[142:143], v[98:99] op_sel_hi:[0,1]
	v_pk_mul_f32 v[106:107], v[142:143], v[96:97] op_sel_hi:[0,1]
	v_pk_mul_f32 v[96:97], v[142:143], v[94:95] op_sel_hi:[0,1]
	v_cvt_pk_bf16_f32 v94, v102, v103
	v_cvt_pk_bf16_f32 v95, v104, v105
	v_cvt_pk_bf16_f32 v96, v96, v97
	v_cvt_pk_bf16_f32 v97, v106, v107
	global_store_dwordx4 v[110:111], v[94:97], off offset:256 sc1
	v_pk_mul_f32 v[86:87], v[142:143], v[86:87] op_sel_hi:[0,1]
	v_pk_mul_f32 v[88:89], v[142:143], v[88:89] op_sel_hi:[0,1]
	v_or_b32_e32 v94, 32, v1
	v_mad_i64_i32 v[94:95], s[22:23], v94, s48, v[144:145]
	v_lshl_add_u64 v[94:95], v[94:95], 0, v[146:147]
	v_pk_mul_f32 v[96:97], v[142:143], v[100:101] op_sel_hi:[0,1]
	v_pk_mul_f32 v[100:101], v[142:143], v[92:93] op_sel_hi:[0,1]
	v_pk_mul_f32 v[92:93], v[142:143], v[90:91] op_sel_hi:[0,1]
	v_cvt_pk_bf16_f32 v90, v98, v99
	v_cvt_pk_bf16_f32 v91, v96, v97
	v_cvt_pk_bf16_f32 v92, v92, v93
	v_cvt_pk_bf16_f32 v93, v100, v101
	global_store_dwordx4 v[94:95], v[90:93], off sc1
	v_pk_mul_f32 v[82:83], v[142:143], v[82:83] op_sel_hi:[0,1]
	v_pk_mul_f32 v[70:71], v[142:143], v[70:71] op_sel_hi:[0,1]
	v_pk_mul_f32 v[90:91], v[142:143], v[80:81] op_sel_hi:[0,1]
	v_pk_mul_f32 v[80:81], v[142:143], v[78:79] op_sel_hi:[0,1]
	v_cvt_pk_bf16_f32 v78, v86, v87
	v_cvt_pk_bf16_f32 v79, v88, v89
	v_cvt_pk_bf16_f32 v80, v80, v81
	v_cvt_pk_bf16_f32 v81, v90, v91
	global_store_dwordx4 v[94:95], v[78:81], off offset:256 sc1
	v_pk_mul_f32 v[72:73], v[142:143], v[72:73] op_sel_hi:[0,1]
	v_pk_mul_f32 v[64:65], v[142:143], v[64:65] op_sel_hi:[0,1]
	v_or_b32_e32 v78, 48, v1
	v_mad_i64_i32 v[78:79], s[22:23], v78, s48, v[144:145]
	v_lshl_add_u64 v[78:79], v[78:79], 0, v[146:147]
	v_pk_mul_f32 v[80:81], v[142:143], v[84:85] op_sel_hi:[0,1]
	v_pk_mul_f32 v[84:85], v[142:143], v[76:77] op_sel_hi:[0,1]
	v_pk_mul_f32 v[76:77], v[142:143], v[74:75] op_sel_hi:[0,1]
	v_cvt_pk_bf16_f32 v74, v82, v83
	v_cvt_pk_bf16_f32 v75, v80, v81
	v_cvt_pk_bf16_f32 v76, v76, v77
	v_cvt_pk_bf16_f32 v77, v84, v85
	global_store_dwordx4 v[78:79], v[74:77], off sc1
	v_pk_mul_f32 v[62:63], v[142:143], v[62:63] op_sel_hi:[0,1]
	v_pk_mul_f32 v[54:55], v[142:143], v[54:55] op_sel_hi:[0,1]
	v_pk_mul_f32 v[74:75], v[142:143], v[68:69] op_sel_hi:[0,1]
	v_pk_mul_f32 v[68:69], v[142:143], v[66:67] op_sel_hi:[0,1]
	v_cvt_pk_bf16_f32 v66, v70, v71
	v_cvt_pk_bf16_f32 v67, v72, v73
	v_cvt_pk_bf16_f32 v68, v68, v69
	v_cvt_pk_bf16_f32 v69, v74, v75
	global_store_dwordx4 v[78:79], v[66:69], off offset:256 sc1
	v_pk_mul_f32 v[56:57], v[142:143], v[56:57] op_sel_hi:[0,1]
	v_pk_mul_f32 v[50:51], v[142:143], v[50:51] op_sel_hi:[0,1]
	v_add_u32_e32 v66, 0x80, v1
	v_mad_i64_i32 v[66:67], s[22:23], v66, s48, v[144:145]
	v_lshl_add_u64 v[66:67], v[66:67], 0, v[146:147]
	v_pk_mul_f32 v[68:69], v[142:143], v[60:61] op_sel_hi:[0,1]
	v_pk_mul_f32 v[60:61], v[142:143], v[58:59] op_sel_hi:[0,1]
	v_cvt_pk_bf16_f32 v58, v62, v63
	v_cvt_pk_bf16_f32 v59, v64, v65
	v_cvt_pk_bf16_f32 v60, v60, v61
	v_cvt_pk_bf16_f32 v61, v68, v69
	global_store_dwordx4 v[66:67], v[58:61], off sc1
	v_pk_mul_f32 v[38:39], v[142:143], v[38:39] op_sel_hi:[0,1]
	v_pk_mul_f32 v[40:41], v[142:143], v[40:41] op_sel_hi:[0,1]
	v_pk_mul_f32 v[58:59], v[142:143], v[48:49] op_sel_hi:[0,1]
	v_pk_mul_f32 v[48:49], v[142:143], v[46:47] op_sel_hi:[0,1]
	v_cvt_pk_bf16_f32 v46, v54, v55
	v_cvt_pk_bf16_f32 v47, v56, v57
	v_cvt_pk_bf16_f32 v48, v48, v49
	v_cvt_pk_bf16_f32 v49, v58, v59
	global_store_dwordx4 v[66:67], v[46:49], off offset:256 sc1
	v_pk_mul_f32 v[34:35], v[142:143], v[34:35] op_sel_hi:[0,1]
	v_pk_mul_f32 v[24:25], v[142:143], v[24:25] op_sel_hi:[0,1]
	v_add_u32_e32 v46, 0x90, v1
	v_mad_i64_i32 v[46:47], s[22:23], v46, s48, v[144:145]
	v_lshl_add_u64 v[46:47], v[46:47], 0, v[146:147]
	v_pk_mul_f32 v[48:49], v[142:143], v[52:53] op_sel_hi:[0,1]
	v_pk_mul_f32 v[52:53], v[142:143], v[44:45] op_sel_hi:[0,1]
	v_pk_mul_f32 v[44:45], v[142:143], v[42:43] op_sel_hi:[0,1]
	v_cvt_pk_bf16_f32 v42, v50, v51
	v_cvt_pk_bf16_f32 v43, v48, v49
	v_cvt_pk_bf16_f32 v44, v44, v45
	v_cvt_pk_bf16_f32 v45, v52, v53
	global_store_dwordx4 v[46:47], v[42:45], off sc1
	v_pk_mul_f32 v[22:23], v[142:143], v[22:23] op_sel_hi:[0,1]
	v_pk_mul_f32 v[18:19], v[142:143], v[18:19] op_sel_hi:[0,1]
	v_pk_mul_f32 v[42:43], v[142:143], v[32:33] op_sel_hi:[0,1]
	v_pk_mul_f32 v[32:33], v[142:143], v[30:31] op_sel_hi:[0,1]
	v_cvt_pk_bf16_f32 v30, v38, v39
	v_cvt_pk_bf16_f32 v31, v40, v41
	v_cvt_pk_bf16_f32 v32, v32, v33
	v_cvt_pk_bf16_f32 v33, v42, v43
	global_store_dwordx4 v[46:47], v[30:33], off offset:256 sc1
	s_and_b64 vcc, exec, s[0:1]
	v_pk_mul_f32 v[8:9], v[142:143], v[8:9] op_sel_hi:[0,1]
	v_add_u32_e32 v30, 0xa0, v1
	v_mad_i64_i32 v[30:31], s[22:23], v30, s48, v[144:145]
	v_lshl_add_u64 v[30:31], v[30:31], 0, v[146:147]
	v_pk_mul_f32 v[32:33], v[142:143], v[36:37] op_sel_hi:[0,1]
	v_pk_mul_f32 v[36:37], v[142:143], v[28:29] op_sel_hi:[0,1]
	v_pk_mul_f32 v[28:29], v[142:143], v[26:27] op_sel_hi:[0,1]
	v_cvt_pk_bf16_f32 v26, v34, v35
	v_cvt_pk_bf16_f32 v27, v32, v33
	v_cvt_pk_bf16_f32 v28, v28, v29
	v_cvt_pk_bf16_f32 v29, v36, v37
	global_store_dwordx4 v[30:31], v[26:29], off sc1
	v_add_u32_e32 v1, 0xb0, v1
	v_pk_mul_f32 v[6:7], v[142:143], v[6:7] op_sel_hi:[0,1]
	v_pk_mul_f32 v[26:27], v[142:143], v[16:17] op_sel_hi:[0,1]
	v_pk_mul_f32 v[16:17], v[142:143], v[14:15] op_sel_hi:[0,1]
	v_cvt_pk_bf16_f32 v14, v22, v23
	v_cvt_pk_bf16_f32 v15, v24, v25
	v_cvt_pk_bf16_f32 v16, v16, v17
	v_cvt_pk_bf16_f32 v17, v26, v27
	global_store_dwordx4 v[30:31], v[14:17], off offset:256 sc1
	s_nop 1
	v_mad_i64_i32 v[14:15], s[22:23], v1, s48, v[144:145]
	v_lshl_add_u64 v[14:15], v[14:15], 0, v[146:147]
	v_pk_mul_f32 v[16:17], v[142:143], v[20:21] op_sel_hi:[0,1]
	v_pk_mul_f32 v[20:21], v[142:143], v[12:13] op_sel_hi:[0,1]
	v_pk_mul_f32 v[12:13], v[142:143], v[10:11] op_sel_hi:[0,1]
	v_cvt_pk_bf16_f32 v10, v18, v19
	v_cvt_pk_bf16_f32 v11, v16, v17
	v_cvt_pk_bf16_f32 v12, v12, v13
	v_cvt_pk_bf16_f32 v13, v20, v21
	global_store_dwordx4 v[14:15], v[10:13], off sc1
	s_nop 1
	v_pk_mul_f32 v[10:11], v[142:143], v[4:5] op_sel_hi:[0,1]
	v_pk_mul_f32 v[4:5], v[142:143], v[2:3] op_sel_hi:[0,1]
	v_cvt_pk_bf16_f32 v2, v6, v7
	v_cvt_pk_bf16_f32 v3, v8, v9
	v_cvt_pk_bf16_f32 v4, v4, v5
	v_cvt_pk_bf16_f32 v5, v10, v11
	global_store_dwordx4 v[14:15], v[2:5], off offset:256 sc1
	s_cbranch_vccnz .LBB0_385
	s_andn2_b64 vcc, exec, s[6:7]
	s_cbranch_vccnz .LBB0_370
	s_barrier
	s_branch .LBB0_370

.LBB0_419:
	v_lshl_add_u32 v14, s2, 8, v212
	v_mov_b64_e32 v[4:5], s[88:89]
	v_ashrrev_i32_e32 v195, 31, v194
	v_mad_i64_i32 v[4:5], s[0:1], v14, s54, v[4:5]
	v_lshl_add_u64 v[4:5], v[194:195], 1, v[4:5]
	v_cvt_pk_bf16_f32 v6, v6, v7
	v_cvt_pk_bf16_f32 v7, v10, v11
	v_cvt_pk_bf16_f32 v8, v8, v9
	v_cvt_pk_bf16_f32 v9, v12, v13
	global_store_dwordx4 v[4:5], v[6:9], off sc1
	s_andn2_b64 vcc, exec, s[30:31]
	s_mov_b64 s[0:1], -1
	v_cndmask_b32_e64 v6, 0, 1, s[30:31]
	v_cmp_ne_u32_e64 s[4:5], 1, v6
	s_cbranch_vccnz .LBB0_421
	v_mov_b32_e32 v8, v2
	v_mov_b32_e32 v9, v2
	v_pk_mul_f32 v[10:11], v[8:9], v[172:173]
	v_pk_mul_f32 v[6:7], v[2:3], v[170:171]
	v_pk_mul_f32 v[12:13], v[8:9], v[168:169]
	v_pk_mul_f32 v[8:9], v[2:3], v[166:167]
	s_mov_b64 s[0:1], 0

.LBB0_423:
	v_cvt_pk_bf16_f32 v6, v6, v7
	v_cvt_pk_bf16_f32 v7, v10, v11
	v_cvt_pk_bf16_f32 v8, v8, v9
	v_cvt_pk_bf16_f32 v9, v12, v13
	s_and_b64 vcc, exec, s[4:5]
	s_mov_b64 s[0:1], -1
	global_store_dwordx4 v[4:5], v[6:9], off offset:256 sc1
	s_cbranch_vccnz .LBB0_425
	v_mov_b32_e32 v4, v2
	v_mov_b32_e32 v5, v2
	v_pk_mul_f32 v[10:11], v[4:5], v[164:165]
	v_pk_mul_f32 v[6:7], v[2:3], v[162:163]
	v_pk_mul_f32 v[12:13], v[4:5], v[160:161]
	v_pk_mul_f32 v[8:9], v[2:3], v[158:159]
	s_mov_b64 s[0:1], 0

.LBB0_427:
	v_or_b32_e32 v15, 16, v14
	v_mov_b64_e32 v[4:5], s[88:89]
	v_mad_i64_i32 v[4:5], s[0:1], v15, s54, v[4:5]
	v_lshl_add_u64 v[4:5], v[194:195], 1, v[4:5]
	v_cvt_pk_bf16_f32 v6, v6, v7
	v_cvt_pk_bf16_f32 v7, v10, v11
	v_cvt_pk_bf16_f32 v8, v8, v9
	v_cvt_pk_bf16_f32 v9, v12, v13
	s_and_b64 vcc, exec, s[4:5]
	s_mov_b64 s[0:1], -1
	global_store_dwordx4 v[4:5], v[6:9], off sc1
	s_cbranch_vccnz .LBB0_429
	s_nop 0
	v_mov_b32_e32 v8, v2
	v_mov_b32_e32 v9, v2
	v_pk_mul_f32 v[10:11], v[8:9], v[156:157]
	v_pk_mul_f32 v[6:7], v[2:3], v[154:155]
	v_pk_mul_f32 v[12:13], v[8:9], v[152:153]
	v_pk_mul_f32 v[8:9], v[2:3], v[150:151]
	s_mov_b64 s[0:1], 0

.LBB0_431:
	v_cvt_pk_bf16_f32 v6, v6, v7
	v_cvt_pk_bf16_f32 v7, v10, v11
	v_cvt_pk_bf16_f32 v8, v8, v9
	v_cvt_pk_bf16_f32 v9, v12, v13
	s_and_b64 vcc, exec, s[4:5]
	s_mov_b64 s[0:1], -1
	global_store_dwordx4 v[4:5], v[6:9], off offset:256 sc1
	s_cbranch_vccnz .LBB0_433
	v_mov_b32_e32 v4, v2
	v_mov_b32_e32 v5, v2
	v_pk_mul_f32 v[10:11], v[4:5], v[148:149]
	v_pk_mul_f32 v[6:7], v[2:3], v[146:147]
	v_pk_mul_f32 v[12:13], v[4:5], v[144:145]
	v_pk_mul_f32 v[8:9], v[2:3], v[142:143]
	s_mov_b64 s[0:1], 0

.LBB0_435:
	v_or_b32_e32 v15, 32, v14
	v_mov_b64_e32 v[4:5], s[88:89]
	v_mad_i64_i32 v[4:5], s[0:1], v15, s54, v[4:5]
	v_lshl_add_u64 v[4:5], v[194:195], 1, v[4:5]
	v_cvt_pk_bf16_f32 v6, v6, v7
	v_cvt_pk_bf16_f32 v7, v10, v11
	v_cvt_pk_bf16_f32 v8, v8, v9
	v_cvt_pk_bf16_f32 v9, v12, v13
	s_and_b64 vcc, exec, s[4:5]
	s_mov_b64 s[0:1], -1
	global_store_dwordx4 v[4:5], v[6:9], off sc1
	s_cbranch_vccnz .LBB0_437
	s_nop 0
	v_mov_b32_e32 v8, v2
	v_mov_b32_e32 v9, v2
	v_pk_mul_f32 v[10:11], v[8:9], v[140:141]
	v_pk_mul_f32 v[6:7], v[2:3], v[138:139]
	v_pk_mul_f32 v[12:13], v[8:9], v[136:137]
	v_pk_mul_f32 v[8:9], v[2:3], v[134:135]
	s_mov_b64 s[0:1], 0

.LBB0_439:
	v_cvt_pk_bf16_f32 v6, v6, v7
	v_cvt_pk_bf16_f32 v7, v10, v11
	v_cvt_pk_bf16_f32 v8, v8, v9
	v_cvt_pk_bf16_f32 v9, v12, v13
	s_and_b64 vcc, exec, s[4:5]
	s_mov_b64 s[0:1], -1
	global_store_dwordx4 v[4:5], v[6:9], off offset:256 sc1
	s_cbranch_vccnz .LBB0_441
	v_mov_b32_e32 v4, v2
	v_mov_b32_e32 v5, v2
	v_pk_mul_f32 v[10:11], v[4:5], v[132:133]
	v_pk_mul_f32 v[6:7], v[2:3], v[130:131]
	v_pk_mul_f32 v[12:13], v[4:5], v[128:129]
	v_pk_mul_f32 v[8:9], v[2:3], v[126:127]
	s_mov_b64 s[0:1], 0

.LBB0_443:
	v_or_b32_e32 v15, 48, v14
	v_mov_b64_e32 v[4:5], s[88:89]
	v_mad_i64_i32 v[4:5], s[0:1], v15, s54, v[4:5]
	v_lshl_add_u64 v[4:5], v[194:195], 1, v[4:5]
	v_cvt_pk_bf16_f32 v6, v6, v7
	v_cvt_pk_bf16_f32 v7, v10, v11
	v_cvt_pk_bf16_f32 v8, v8, v9
	v_cvt_pk_bf16_f32 v9, v12, v13
	s_and_b64 vcc, exec, s[4:5]
	s_mov_b64 s[0:1], -1
	global_store_dwordx4 v[4:5], v[6:9], off sc1
	s_cbranch_vccnz .LBB0_445
	s_nop 0
	v_mov_b32_e32 v8, v2
	v_mov_b32_e32 v9, v2
	v_pk_mul_f32 v[10:11], v[8:9], v[124:125]
	v_pk_mul_f32 v[6:7], v[2:3], v[122:123]
	v_pk_mul_f32 v[12:13], v[8:9], v[120:121]
	v_pk_mul_f32 v[8:9], v[2:3], v[118:119]
	s_mov_b64 s[0:1], 0

.LBB0_447:
	v_cvt_pk_bf16_f32 v6, v6, v7
	v_cvt_pk_bf16_f32 v7, v10, v11
	v_cvt_pk_bf16_f32 v8, v8, v9
	v_cvt_pk_bf16_f32 v9, v12, v13
	s_and_b64 vcc, exec, s[4:5]
	s_mov_b64 s[0:1], -1
	global_store_dwordx4 v[4:5], v[6:9], off offset:256 sc1
	s_cbranch_vccnz .LBB0_449
	v_mov_b32_e32 v4, v2
	v_mov_b32_e32 v5, v2
	v_pk_mul_f32 v[10:11], v[4:5], v[116:117]
	v_pk_mul_f32 v[6:7], v[2:3], v[114:115]
	v_pk_mul_f32 v[12:13], v[4:5], v[112:113]
	v_pk_mul_f32 v[8:9], v[2:3], v[110:111]
	s_mov_b64 s[0:1], 0

.LBB0_451:
	v_add_u32_e32 v15, 0x80, v14
	v_mov_b64_e32 v[4:5], s[88:89]
	v_mad_i64_i32 v[4:5], s[0:1], v15, s54, v[4:5]
	v_lshl_add_u64 v[4:5], v[194:195], 1, v[4:5]
	v_cvt_pk_bf16_f32 v6, v6, v7
	v_cvt_pk_bf16_f32 v7, v10, v11
	v_cvt_pk_bf16_f32 v8, v8, v9
	v_cvt_pk_bf16_f32 v9, v12, v13
	s_and_b64 vcc, exec, s[4:5]
	s_mov_b64 s[0:1], -1
	global_store_dwordx4 v[4:5], v[6:9], off sc1
	s_cbranch_vccnz .LBB0_453
	s_nop 0
	v_mov_b32_e32 v8, v2
	v_mov_b32_e32 v9, v2
	v_pk_mul_f32 v[10:11], v[8:9], v[108:109]
	v_pk_mul_f32 v[6:7], v[2:3], v[106:107]
	v_pk_mul_f32 v[12:13], v[8:9], v[104:105]
	v_pk_mul_f32 v[8:9], v[2:3], v[102:103]
	s_mov_b64 s[0:1], 0

.LBB0_455:
	v_cvt_pk_bf16_f32 v6, v6, v7
	v_cvt_pk_bf16_f32 v7, v10, v11
	v_cvt_pk_bf16_f32 v8, v8, v9
	v_cvt_pk_bf16_f32 v9, v12, v13
	s_and_b64 vcc, exec, s[4:5]
	s_mov_b64 s[0:1], -1
	global_store_dwordx4 v[4:5], v[6:9], off offset:256 sc1
	s_cbranch_vccnz .LBB0_457
	v_mov_b32_e32 v4, v2
	v_mov_b32_e32 v5, v2
	v_pk_mul_f32 v[10:11], v[4:5], v[100:101]
	v_pk_mul_f32 v[6:7], v[2:3], v[98:99]
	v_pk_mul_f32 v[12:13], v[4:5], v[96:97]
	v_pk_mul_f32 v[8:9], v[2:3], v[94:95]
	s_mov_b64 s[0:1], 0

.LBB0_459:
	v_add_u32_e32 v15, 0x90, v14
	v_mov_b64_e32 v[4:5], s[88:89]
	v_mad_i64_i32 v[4:5], s[0:1], v15, s54, v[4:5]
	v_lshl_add_u64 v[4:5], v[194:195], 1, v[4:5]
	v_cvt_pk_bf16_f32 v6, v6, v7
	v_cvt_pk_bf16_f32 v7, v10, v11
	v_cvt_pk_bf16_f32 v8, v8, v9
	v_cvt_pk_bf16_f32 v9, v12, v13
	s_and_b64 vcc, exec, s[4:5]
	s_mov_b64 s[0:1], -1
	global_store_dwordx4 v[4:5], v[6:9], off sc1
	s_cbranch_vccnz .LBB0_461
	s_nop 0
	v_mov_b32_e32 v8, v2
	v_mov_b32_e32 v9, v2
	v_pk_mul_f32 v[10:11], v[8:9], v[92:93]
	v_pk_mul_f32 v[6:7], v[2:3], v[90:91]
	v_pk_mul_f32 v[12:13], v[8:9], v[88:89]
	v_pk_mul_f32 v[8:9], v[2:3], v[86:87]
	s_mov_b64 s[0:1], 0

.LBB0_463:
	v_cvt_pk_bf16_f32 v6, v6, v7
	v_cvt_pk_bf16_f32 v7, v10, v11
	v_cvt_pk_bf16_f32 v8, v8, v9
	v_cvt_pk_bf16_f32 v9, v12, v13
	s_and_b64 vcc, exec, s[4:5]
	s_mov_b64 s[0:1], -1
	global_store_dwordx4 v[4:5], v[6:9], off offset:256 sc1
	s_cbranch_vccnz .LBB0_465
	v_mov_b32_e32 v4, v2
	v_mov_b32_e32 v5, v2
	v_pk_mul_f32 v[10:11], v[4:5], v[84:85]
	v_pk_mul_f32 v[6:7], v[2:3], v[82:83]
	v_pk_mul_f32 v[12:13], v[4:5], v[80:81]
	v_pk_mul_f32 v[8:9], v[2:3], v[78:79]
	s_mov_b64 s[0:1], 0

.LBB0_467:
	v_add_u32_e32 v15, 0xa0, v14
	v_mov_b64_e32 v[4:5], s[88:89]
	v_mad_i64_i32 v[4:5], s[0:1], v15, s54, v[4:5]
	v_lshl_add_u64 v[4:5], v[194:195], 1, v[4:5]
	v_cvt_pk_bf16_f32 v6, v6, v7
	v_cvt_pk_bf16_f32 v7, v10, v11
	v_cvt_pk_bf16_f32 v8, v8, v9
	v_cvt_pk_bf16_f32 v9, v12, v13
	s_and_b64 vcc, exec, s[4:5]
	s_mov_b64 s[0:1], -1
	global_store_dwordx4 v[4:5], v[6:9], off sc1
	s_cbranch_vccnz .LBB0_469
	s_nop 0
	v_mov_b32_e32 v8, v2
	v_mov_b32_e32 v9, v2
	v_pk_mul_f32 v[10:11], v[8:9], v[76:77]
	v_pk_mul_f32 v[6:7], v[2:3], v[74:75]
	v_pk_mul_f32 v[12:13], v[8:9], v[72:73]
	v_pk_mul_f32 v[8:9], v[2:3], v[70:71]
	s_mov_b64 s[0:1], 0

.LBB0_471:
	v_cvt_pk_bf16_f32 v6, v6, v7
	v_cvt_pk_bf16_f32 v7, v10, v11
	v_cvt_pk_bf16_f32 v8, v8, v9
	v_cvt_pk_bf16_f32 v9, v12, v13
	s_and_b64 vcc, exec, s[4:5]
	s_mov_b64 s[0:1], -1
	global_store_dwordx4 v[4:5], v[6:9], off offset:256 sc1
	s_cbranch_vccnz .LBB0_473
	v_mov_b32_e32 v4, v2
	v_mov_b32_e32 v5, v2
	v_pk_mul_f32 v[10:11], v[4:5], v[68:69]
	v_pk_mul_f32 v[6:7], v[2:3], v[66:67]
	v_pk_mul_f32 v[12:13], v[4:5], v[64:65]
	v_pk_mul_f32 v[8:9], v[2:3], v[62:63]
	s_mov_b64 s[0:1], 0

.LBB0_475:
	v_add_u32_e32 v14, 0xb0, v14
	v_mov_b64_e32 v[4:5], s[88:89]
	v_mad_i64_i32 v[4:5], s[0:1], v14, s54, v[4:5]
	v_lshl_add_u64 v[4:5], v[194:195], 1, v[4:5]
	v_cvt_pk_bf16_f32 v6, v6, v7
	v_cvt_pk_bf16_f32 v7, v10, v11
	v_cvt_pk_bf16_f32 v8, v8, v9
	v_cvt_pk_bf16_f32 v9, v12, v13
	s_and_b64 vcc, exec, s[4:5]
	s_mov_b64 s[0:1], -1
	global_store_dwordx4 v[4:5], v[6:9], off sc1
	s_cbranch_vccnz .LBB0_477
	s_nop 0
	v_mov_b32_e32 v8, v2
	v_mov_b32_e32 v9, v2
	v_pk_mul_f32 v[10:11], v[8:9], v[60:61]
	v_pk_mul_f32 v[6:7], v[2:3], v[58:59]
	v_pk_mul_f32 v[12:13], v[8:9], v[56:57]
	v_pk_mul_f32 v[8:9], v[2:3], v[54:55]
	s_mov_b64 s[0:1], 0

.LBB0_479:
	s_and_b64 vcc, exec, s[6:7]
	v_cvt_pk_bf16_f32 v6, v6, v7
	v_cvt_pk_bf16_f32 v7, v10, v11
	v_cvt_pk_bf16_f32 v8, v8, v9
	v_cvt_pk_bf16_f32 v9, v12, v13
	global_store_dwordx4 v[4:5], v[6:9], off offset:256 sc1
	s_cbranch_vccnz .LBB0_482
	s_andn2_b64 vcc, exec, s[18:19]
	s_cbranch_vccnz .LBB0_393
	s_barrier
	s_branch .LBB0_393

.LBB0_923:
	v_mul_lo_u32 v143, v221, s41
	v_lshl_add_u32 v143, v206, 1, v143
	v_add_u32_e32 v143, 0x2000, v143
	s_mov_b64 s[98:99], s[12:13]
	global_load_dwordx4 v[144:147], v143, s[98:99]
	global_load_dwordx4 v[148:151], v143, s[98:99] offset:256
	s_add_u32 s98, s98, 0x68800
	s_addc_u32 s99, s99, 0
	global_load_dwordx4 v[152:155], v143, s[98:99]
	global_load_dwordx4 v[156:159], v143, s[98:99] offset:256
	s_add_u32 s98, s98, 0x68800
	s_addc_u32 s99, s99, 0
	global_load_dwordx4 v[160:163], v143, s[98:99]
	global_load_dwordx4 v[164:167], v143, s[98:99] offset:256
	s_add_u32 s98, s98, 0x68800
	s_addc_u32 s99, s99, 0
	global_load_dwordx4 v[168:171], v143, s[98:99]
	global_load_dwordx4 v[172:175], v143, s[98:99] offset:256
	s_add_u32 s98, s98, 0x20a800
	s_addc_u32 s99, s99, 0
	global_load_dwordx4 v[176:179], v143, s[98:99]
	global_load_dwordx4 v[180:183], v143, s[98:99] offset:256
	s_add_u32 s98, s98, 0x68800
	s_addc_u32 s99, s99, 0
	global_load_dwordx4 v[184:187], v143, s[98:99]
	global_load_dwordx4 v[188:191], v143, s[98:99] offset:256
	s_add_u32 s98, s98, 0x68800
	s_addc_u32 s99, s99, 0
	global_load_dwordx4 v[222:225], v143, s[98:99]
	global_load_dwordx4 v[226:229], v143, s[98:99] offset:256
	s_add_u32 s98, s98, 0x68800
	s_addc_u32 s99, s99, 0
	global_load_dwordx4 v[230:233], v143, s[98:99]
	global_load_dwordx4 v[234:237], v143, s[98:99] offset:256
	v_mov_b64_e32 v[132:133], s[12:13]
	v_mad_i64_i32 v[134:135], s[22:23], v221, s41, v[132:133]
	v_lshlrev_b64 v[130:131], 1, v[206:207]
	v_lshl_add_u64 v[134:135], v[134:135], 0, v[130:131]
	v_add_co_u32_e32 v138, vcc, 0x2000, v134
	s_nop 1
	v_addc_co_u32_e32 v139, vcc, 0, v135, vcc
	s_waitcnt vmcnt(15)
	v_lshlrev_b32_e32 v1, 16, v144
	v_and_b32_e32 v134, 0xffff0000, v144
	v_lshlrev_b32_e32 v140, 16, v145
	v_lshlrev_b32_e32 v142, 16, v147
	v_and_b32_e32 v137, 0xffff0000, v147
	v_and_b32_e32 v135, 0xffff0000, v145
	v_lshlrev_b32_e32 v141, 16, v146
	v_and_b32_e32 v136, 0xffff0000, v146
	v_mul_f32_e32 v1, v126, v1
	v_mul_f32_e32 v126, v127, v134
	v_mul_f32_e32 v127, v128, v140
	v_mul_f32_e32 v134, v125, v137
	v_mul_f32_e32 v128, v129, v135
	v_mul_f32_e32 v122, v122, v141
	v_mul_f32_e32 v123, v123, v136
	v_mul_f32_e32 v129, v124, v142
	v_cvt_pk_bf16_f32 v124, v1, v126
	v_cvt_pk_bf16_f32 v125, v127, v128
	v_cvt_pk_bf16_f32 v126, v122, v123
	v_cvt_pk_bf16_f32 v127, v129, v134
	v_mov_b64_e32 v[122:123], s[4:5]
	v_or_b32_e32 v1, 16, v221
	v_mad_i64_i32 v[128:129], s[22:23], v221, s46, v[122:123]
	v_mad_i64_i32 v[138:139], s[22:23], v1, s41, v[132:133]
	v_lshl_add_u64 v[128:129], v[128:129], 0, v[130:131]
	v_lshl_add_u64 v[138:139], v[138:139], 0, v[130:131]
	v_add_co_u32_e32 v138, vcc, s39, v138
	global_store_dwordx4 v[128:129], v[124:127], off sc1
	s_nop 0
	v_addc_co_u32_e32 v139, vcc, 0, v139, vcc
	s_waitcnt vmcnt(15)
	v_lshlrev_b32_e32 v124, 16, v148
	v_and_b32_e32 v125, 0xffff0000, v148
	v_lshlrev_b32_e32 v126, 16, v149
	v_and_b32_e32 v127, 0xffff0000, v149
	v_lshlrev_b32_e32 v134, 16, v150
	v_and_b32_e32 v135, 0xffff0000, v150
	v_lshlrev_b32_e32 v136, 16, v151
	v_and_b32_e32 v137, 0xffff0000, v151
	v_mul_f32_e32 v118, v118, v124
	v_mul_f32_e32 v119, v119, v125
	v_mul_f32_e32 v120, v120, v126
	v_mul_f32_e32 v121, v121, v127
	v_mul_f32_e32 v113, v113, v137
	v_mul_f32_e32 v124, v110, v134
	v_mul_f32_e32 v125, v111, v135
	v_mul_f32_e32 v126, v112, v136
	v_cvt_pk_bf16_f32 v110, v118, v119
	v_cvt_pk_bf16_f32 v111, v120, v121
	v_cvt_pk_bf16_f32 v112, v124, v125
	v_cvt_pk_bf16_f32 v113, v126, v113
	s_nop 0
	global_store_dwordx4 v[128:129], v[110:113], off offset:256 sc1
	s_waitcnt vmcnt(15)
	s_nop 0
	v_lshlrev_b32_e32 v110, 16, v152
	v_and_b32_e32 v111, 0xffff0000, v152
	v_lshlrev_b32_e32 v112, 16, v153
	v_and_b32_e32 v113, 0xffff0000, v153
	v_lshlrev_b32_e32 v118, 16, v154
	v_and_b32_e32 v119, 0xffff0000, v154
	v_lshlrev_b32_e32 v120, 16, v155
	v_and_b32_e32 v121, 0xffff0000, v155
	v_mul_f32_e32 v110, v114, v110
	v_mul_f32_e32 v111, v115, v111
	v_mul_f32_e32 v112, v116, v112
	v_mul_f32_e32 v113, v117, v113
	v_mul_f32_e32 v109, v109, v121
	v_mul_f32_e32 v114, v106, v118
	v_mul_f32_e32 v115, v107, v119
	v_mul_f32_e32 v116, v108, v120
	v_cvt_pk_bf16_f32 v106, v110, v111
	v_cvt_pk_bf16_f32 v107, v112, v113
	v_cvt_pk_bf16_f32 v108, v114, v115
	v_cvt_pk_bf16_f32 v109, v116, v109
	v_or_b32_e32 v118, 32, v221
	v_mad_i64_i32 v[114:115], s[22:23], v1, s46, v[122:123]
	v_mad_i64_i32 v[116:117], s[22:23], v118, s41, v[132:133]
	v_lshl_add_u64 v[114:115], v[114:115], 0, v[130:131]
	v_lshl_add_u64 v[116:117], v[116:117], 0, v[130:131]
	v_add_co_u32_e32 v116, vcc, s39, v116
	global_store_dwordx4 v[114:115], v[106:109], off sc1
	s_nop 0
	v_addc_co_u32_e32 v117, vcc, 0, v117, vcc
	s_waitcnt vmcnt(15)
	v_lshlrev_b32_e32 v1, 16, v156
	v_and_b32_e32 v106, 0xffff0000, v156
	v_lshlrev_b32_e32 v107, 16, v157
	v_and_b32_e32 v108, 0xffff0000, v157
	v_lshlrev_b32_e32 v109, 16, v158
	v_and_b32_e32 v110, 0xffff0000, v158
	v_and_b32_e32 v112, 0xffff0000, v159
	v_lshlrev_b32_e32 v111, 16, v159
	v_mul_f32_e32 v1, v102, v1
	v_mul_f32_e32 v102, v103, v106
	v_mul_f32_e32 v103, v104, v107
	v_mul_f32_e32 v104, v105, v108
	v_mul_f32_e32 v105, v94, v109
	v_mul_f32_e32 v97, v97, v112
	v_mul_f32_e32 v106, v95, v110
	v_mul_f32_e32 v107, v96, v111
	v_cvt_pk_bf16_f32 v94, v1, v102
	v_cvt_pk_bf16_f32 v95, v103, v104
	v_cvt_pk_bf16_f32 v96, v105, v106
	v_cvt_pk_bf16_f32 v97, v107, v97
	s_waitcnt vmcnt(15)
	v_lshlrev_b32_e32 v1, 16, v160
	global_store_dwordx4 v[114:115], v[94:97], off offset:256 sc1
	v_mul_f32_e32 v1, v98, v1
	s_nop 0
	v_and_b32_e32 v94, 0xffff0000, v160
	v_lshlrev_b32_e32 v95, 16, v161
	v_and_b32_e32 v96, 0xffff0000, v161
	v_lshlrev_b32_e32 v97, 16, v162
	v_and_b32_e32 v102, 0xffff0000, v162
	v_and_b32_e32 v104, 0xffff0000, v163
	v_lshlrev_b32_e32 v103, 16, v163
	v_mul_f32_e32 v94, v99, v94
	v_mul_f32_e32 v95, v100, v95
	v_mul_f32_e32 v96, v101, v96
	v_mul_f32_e32 v97, v90, v97
	v_mul_f32_e32 v93, v93, v104
	v_mul_f32_e32 v98, v91, v102
	v_mul_f32_e32 v99, v92, v103
	v_cvt_pk_bf16_f32 v90, v1, v94
	v_cvt_pk_bf16_f32 v91, v95, v96
	v_cvt_pk_bf16_f32 v92, v97, v98
	v_cvt_pk_bf16_f32 v93, v99, v93
	v_or_b32_e32 v1, 48, v221
	v_mad_i64_i32 v[98:99], s[22:23], v118, s46, v[122:123]
	v_mad_i64_i32 v[100:101], s[22:23], v1, s41, v[132:133]
	v_lshl_add_u64 v[98:99], v[98:99], 0, v[130:131]
	v_lshl_add_u64 v[100:101], v[100:101], 0, v[130:131]
	v_add_co_u32_e32 v100, vcc, s39, v100
	global_store_dwordx4 v[98:99], v[90:93], off sc1
	s_nop 0
	v_addc_co_u32_e32 v101, vcc, 0, v101, vcc
	s_waitcnt vmcnt(15)
	v_lshlrev_b32_e32 v90, 16, v164
	v_and_b32_e32 v91, 0xffff0000, v164
	v_lshlrev_b32_e32 v92, 16, v165
	v_and_b32_e32 v93, 0xffff0000, v165
	v_lshlrev_b32_e32 v94, 16, v166
	v_and_b32_e32 v95, 0xffff0000, v166
	v_lshlrev_b32_e32 v96, 16, v167
	v_and_b32_e32 v97, 0xffff0000, v167
	v_mul_f32_e32 v86, v86, v90
	v_mul_f32_e32 v87, v87, v91
	v_mul_f32_e32 v88, v88, v92
	v_mul_f32_e32 v89, v89, v93
	v_mul_f32_e32 v81, v81, v97
	v_mul_f32_e32 v90, v78, v94
	v_mul_f32_e32 v91, v79, v95
	v_mul_f32_e32 v92, v80, v96
	v_cvt_pk_bf16_f32 v78, v86, v87
	v_cvt_pk_bf16_f32 v79, v88, v89
	v_cvt_pk_bf16_f32 v80, v90, v91
	v_cvt_pk_bf16_f32 v81, v92, v81
	s_nop 0
	global_store_dwordx4 v[98:99], v[78:81], off offset:256 sc1
	s_waitcnt vmcnt(15)
	s_nop 0
	v_lshlrev_b32_e32 v78, 16, v168
	v_and_b32_e32 v79, 0xffff0000, v168
	v_lshlrev_b32_e32 v80, 16, v169
	v_and_b32_e32 v81, 0xffff0000, v169
	v_lshlrev_b32_e32 v86, 16, v170
	v_and_b32_e32 v87, 0xffff0000, v170
	v_lshlrev_b32_e32 v88, 16, v171
	v_and_b32_e32 v89, 0xffff0000, v171
	v_mul_f32_e32 v78, v82, v78
	v_mul_f32_e32 v79, v83, v79
	v_mul_f32_e32 v80, v84, v80
	v_mul_f32_e32 v81, v85, v81
	v_mul_f32_e32 v77, v77, v89
	v_mul_f32_e32 v82, v74, v86
	v_mul_f32_e32 v83, v75, v87
	v_mul_f32_e32 v84, v76, v88
	v_cvt_pk_bf16_f32 v74, v78, v79
	v_cvt_pk_bf16_f32 v75, v80, v81
	v_cvt_pk_bf16_f32 v76, v82, v83
	v_cvt_pk_bf16_f32 v77, v84, v77
	v_add_u32_e32 v86, 0x80, v221
	v_mad_i64_i32 v[82:83], s[22:23], v1, s46, v[122:123]
	v_mad_i64_i32 v[84:85], s[22:23], v86, s41, v[132:133]
	v_lshl_add_u64 v[82:83], v[82:83], 0, v[130:131]
	v_lshl_add_u64 v[84:85], v[84:85], 0, v[130:131]
	v_add_co_u32_e32 v84, vcc, s39, v84
	global_store_dwordx4 v[82:83], v[74:77], off sc1
	s_nop 0
	v_addc_co_u32_e32 v85, vcc, 0, v85, vcc
	s_waitcnt vmcnt(15)
	v_lshlrev_b32_e32 v1, 16, v172
	v_and_b32_e32 v74, 0xffff0000, v172
	v_lshlrev_b32_e32 v75, 16, v173
	v_and_b32_e32 v76, 0xffff0000, v173
	v_lshlrev_b32_e32 v77, 16, v174
	v_and_b32_e32 v78, 0xffff0000, v174
	v_and_b32_e32 v80, 0xffff0000, v175
	v_lshlrev_b32_e32 v79, 16, v175
	v_mul_f32_e32 v1, v70, v1
	v_mul_f32_e32 v70, v71, v74
	v_mul_f32_e32 v71, v72, v75
	v_mul_f32_e32 v72, v73, v76
	v_mul_f32_e32 v73, v66, v77
	v_mul_f32_e32 v69, v69, v80
	v_mul_f32_e32 v74, v67, v78
	v_mul_f32_e32 v75, v68, v79
	v_cvt_pk_bf16_f32 v66, v1, v70
	v_cvt_pk_bf16_f32 v67, v71, v72
	v_cvt_pk_bf16_f32 v68, v73, v74
	v_cvt_pk_bf16_f32 v69, v75, v69
	s_waitcnt vmcnt(15)
	v_lshlrev_b32_e32 v1, 16, v176
	global_store_dwordx4 v[82:83], v[66:69], off offset:256 sc1
	v_mul_f32_e32 v1, v62, v1
	s_nop 0
	v_and_b32_e32 v66, 0xffff0000, v176
	v_lshlrev_b32_e32 v67, 16, v177
	v_and_b32_e32 v68, 0xffff0000, v177
	v_lshlrev_b32_e32 v69, 16, v178
	v_and_b32_e32 v70, 0xffff0000, v178
	v_and_b32_e32 v72, 0xffff0000, v179
	v_lshlrev_b32_e32 v71, 16, v179
	v_mul_f32_e32 v62, v63, v66
	v_mul_f32_e32 v63, v64, v67
	v_mul_f32_e32 v64, v65, v68
	v_mul_f32_e32 v65, v58, v69
	v_mul_f32_e32 v61, v61, v72
	v_mul_f32_e32 v66, v59, v70
	v_mul_f32_e32 v67, v60, v71
	v_cvt_pk_bf16_f32 v58, v1, v62
	v_cvt_pk_bf16_f32 v59, v63, v64
	v_cvt_pk_bf16_f32 v60, v65, v66
	v_cvt_pk_bf16_f32 v61, v67, v61
	v_add_u32_e32 v1, 0x90, v221
	v_mad_i64_i32 v[66:67], s[22:23], v86, s46, v[122:123]
	v_mad_i64_i32 v[68:69], s[22:23], v1, s41, v[132:133]
	v_lshl_add_u64 v[66:67], v[66:67], 0, v[130:131]
	v_lshl_add_u64 v[68:69], v[68:69], 0, v[130:131]
	v_add_co_u32_e32 v68, vcc, s39, v68
	global_store_dwordx4 v[66:67], v[58:61], off sc1
	s_nop 0
	v_addc_co_u32_e32 v69, vcc, 0, v69, vcc
	s_waitcnt vmcnt(15)
	v_lshlrev_b32_e32 v58, 16, v180
	v_and_b32_e32 v59, 0xffff0000, v180
	v_lshlrev_b32_e32 v60, 16, v181
	v_and_b32_e32 v61, 0xffff0000, v181
	v_lshlrev_b32_e32 v62, 16, v182
	v_and_b32_e32 v63, 0xffff0000, v182
	v_lshlrev_b32_e32 v64, 16, v183
	v_and_b32_e32 v65, 0xffff0000, v183
	v_mul_f32_e32 v54, v54, v58
	v_mul_f32_e32 v55, v55, v59
	v_mul_f32_e32 v56, v56, v60
	v_mul_f32_e32 v57, v57, v61
	v_mul_f32_e32 v49, v49, v65
	v_mul_f32_e32 v58, v46, v62
	v_mul_f32_e32 v59, v47, v63
	v_mul_f32_e32 v60, v48, v64
	v_cvt_pk_bf16_f32 v46, v54, v55
	v_cvt_pk_bf16_f32 v47, v56, v57
	v_cvt_pk_bf16_f32 v48, v58, v59
	v_cvt_pk_bf16_f32 v49, v60, v49
	s_nop 0
	global_store_dwordx4 v[66:67], v[46:49], off offset:256 sc1
	s_waitcnt vmcnt(15)
	s_nop 0
	v_lshlrev_b32_e32 v46, 16, v184
	v_and_b32_e32 v47, 0xffff0000, v184
	v_lshlrev_b32_e32 v48, 16, v185
	v_and_b32_e32 v49, 0xffff0000, v185
	v_lshlrev_b32_e32 v54, 16, v186
	v_and_b32_e32 v55, 0xffff0000, v186
	v_lshlrev_b32_e32 v56, 16, v187
	v_and_b32_e32 v57, 0xffff0000, v187
	v_mul_f32_e32 v46, v50, v46
	v_mul_f32_e32 v47, v51, v47
	v_mul_f32_e32 v48, v52, v48
	v_mul_f32_e32 v49, v53, v49
	v_mul_f32_e32 v45, v45, v57
	v_mul_f32_e32 v50, v42, v54
	v_mul_f32_e32 v51, v43, v55
	v_mul_f32_e32 v52, v44, v56
	v_cvt_pk_bf16_f32 v42, v46, v47
	v_cvt_pk_bf16_f32 v43, v48, v49
	v_cvt_pk_bf16_f32 v44, v50, v51
	v_cvt_pk_bf16_f32 v45, v52, v45
	v_add_u32_e32 v54, 0xa0, v221
	v_mad_i64_i32 v[50:51], s[22:23], v1, s46, v[122:123]
	v_mad_i64_i32 v[52:53], s[22:23], v54, s41, v[132:133]
	v_lshl_add_u64 v[50:51], v[50:51], 0, v[130:131]
	v_lshl_add_u64 v[52:53], v[52:53], 0, v[130:131]
	v_add_co_u32_e32 v52, vcc, s39, v52
	global_store_dwordx4 v[50:51], v[42:45], off sc1
	s_nop 0
	v_addc_co_u32_e32 v53, vcc, 0, v53, vcc
	s_waitcnt vmcnt(15)
	v_lshlrev_b32_e32 v1, 16, v188
	v_and_b32_e32 v42, 0xffff0000, v188
	v_lshlrev_b32_e32 v43, 16, v189
	v_and_b32_e32 v44, 0xffff0000, v189
	v_lshlrev_b32_e32 v45, 16, v190
	v_and_b32_e32 v46, 0xffff0000, v190
	v_and_b32_e32 v48, 0xffff0000, v191
	v_lshlrev_b32_e32 v47, 16, v191
	v_mul_f32_e32 v1, v38, v1
	v_mul_f32_e32 v38, v39, v42
	v_mul_f32_e32 v39, v40, v43
	v_mul_f32_e32 v40, v41, v44
	v_mul_f32_e32 v41, v30, v45
	v_mul_f32_e32 v33, v33, v48
	v_mul_f32_e32 v42, v31, v46
	v_mul_f32_e32 v43, v32, v47
	v_cvt_pk_bf16_f32 v30, v1, v38
	v_cvt_pk_bf16_f32 v31, v39, v40
	v_cvt_pk_bf16_f32 v32, v41, v42
	v_cvt_pk_bf16_f32 v33, v43, v33
	s_waitcnt vmcnt(15)
	v_lshlrev_b32_e32 v1, 16, v222
	global_store_dwordx4 v[50:51], v[30:33], off offset:256 sc1
	v_mul_f32_e32 v1, v34, v1
	s_nop 0
	v_and_b32_e32 v30, 0xffff0000, v222
	v_lshlrev_b32_e32 v31, 16, v223
	v_and_b32_e32 v32, 0xffff0000, v223
	v_lshlrev_b32_e32 v33, 16, v224
	v_and_b32_e32 v38, 0xffff0000, v224
	v_and_b32_e32 v40, 0xffff0000, v225
	v_lshlrev_b32_e32 v39, 16, v225
	v_mul_f32_e32 v30, v35, v30
	v_mul_f32_e32 v31, v36, v31
	v_mul_f32_e32 v32, v37, v32
	v_mul_f32_e32 v33, v26, v33
	v_mul_f32_e32 v29, v29, v40
	v_mul_f32_e32 v34, v27, v38
	v_mul_f32_e32 v35, v28, v39
	v_cvt_pk_bf16_f32 v26, v1, v30
	v_cvt_pk_bf16_f32 v27, v31, v32
	v_cvt_pk_bf16_f32 v28, v33, v34
	v_cvt_pk_bf16_f32 v29, v35, v29
	v_add_u32_e32 v1, 0xb0, v221
	v_mad_i64_i32 v[34:35], s[22:23], v54, s46, v[122:123]
	v_mad_i64_i32 v[36:37], s[22:23], v1, s41, v[132:133]
	v_lshl_add_u64 v[34:35], v[34:35], 0, v[130:131]
	v_lshl_add_u64 v[36:37], v[36:37], 0, v[130:131]
	v_add_co_u32_e32 v36, vcc, s39, v36
	global_store_dwordx4 v[34:35], v[26:29], off sc1
	s_nop 0
	v_addc_co_u32_e32 v37, vcc, 0, v37, vcc
	s_and_b64 vcc, exec, s[0:1]
	s_waitcnt vmcnt(15)
	v_lshlrev_b32_e32 v26, 16, v226
	v_and_b32_e32 v27, 0xffff0000, v226
	v_lshlrev_b32_e32 v28, 16, v227
	v_and_b32_e32 v29, 0xffff0000, v227
	v_lshlrev_b32_e32 v30, 16, v228
	v_and_b32_e32 v31, 0xffff0000, v228
	v_lshlrev_b32_e32 v32, 16, v229
	v_and_b32_e32 v33, 0xffff0000, v229
	v_mul_f32_e32 v22, v22, v26
	v_mul_f32_e32 v23, v23, v27
	v_mul_f32_e32 v24, v24, v28
	v_mul_f32_e32 v25, v25, v29
	v_mul_f32_e32 v17, v17, v33
	v_mul_f32_e32 v26, v14, v30
	v_mul_f32_e32 v27, v15, v31
	v_mul_f32_e32 v28, v16, v32
	v_cvt_pk_bf16_f32 v14, v22, v23
	v_cvt_pk_bf16_f32 v15, v24, v25
	v_cvt_pk_bf16_f32 v16, v26, v27
	v_cvt_pk_bf16_f32 v17, v28, v17
	s_nop 0
	global_store_dwordx4 v[34:35], v[14:17], off offset:256 sc1
	s_waitcnt vmcnt(15)
	s_nop 0
	v_lshlrev_b32_e32 v14, 16, v230
	v_and_b32_e32 v15, 0xffff0000, v230
	v_lshlrev_b32_e32 v16, 16, v231
	v_and_b32_e32 v17, 0xffff0000, v231
	v_lshlrev_b32_e32 v22, 16, v232
	v_and_b32_e32 v23, 0xffff0000, v232
	v_lshlrev_b32_e32 v24, 16, v233
	v_and_b32_e32 v25, 0xffff0000, v233
	v_mul_f32_e32 v14, v18, v14
	v_mul_f32_e32 v15, v19, v15
	v_mul_f32_e32 v16, v20, v16
	v_mul_f32_e32 v17, v21, v17
	v_mul_f32_e32 v13, v13, v25
	v_mul_f32_e32 v18, v10, v22
	v_mul_f32_e32 v19, v11, v23
	v_mul_f32_e32 v20, v12, v24
	v_cvt_pk_bf16_f32 v10, v14, v15
	v_cvt_pk_bf16_f32 v11, v16, v17
	v_cvt_pk_bf16_f32 v12, v18, v19
	v_cvt_pk_bf16_f32 v13, v20, v13
	v_mad_i64_i32 v[18:19], s[22:23], v1, s46, v[122:123]
	v_lshl_add_u64 v[18:19], v[18:19], 0, v[130:131]
	global_store_dwordx4 v[18:19], v[10:13], off sc1
	s_waitcnt vmcnt(15)
	v_lshlrev_b32_e32 v1, 16, v234
	v_and_b32_e32 v10, 0xffff0000, v234
	v_lshlrev_b32_e32 v13, 16, v236
	v_and_b32_e32 v14, 0xffff0000, v236
	v_and_b32_e32 v16, 0xffff0000, v237
	v_lshlrev_b32_e32 v11, 16, v235
	v_and_b32_e32 v12, 0xffff0000, v235
	v_lshlrev_b32_e32 v15, 16, v237
	v_mul_f32_e32 v5, v5, v16
	v_mul_f32_e32 v1, v6, v1
	v_mul_f32_e32 v6, v7, v10
	v_mul_f32_e32 v7, v8, v11
	v_mul_f32_e32 v8, v9, v12
	v_mul_f32_e32 v9, v2, v13
	v_mul_f32_e32 v10, v3, v14
	v_mul_f32_e32 v11, v4, v15
	v_cvt_pk_bf16_f32 v2, v1, v6
	v_cvt_pk_bf16_f32 v3, v7, v8
	v_cvt_pk_bf16_f32 v4, v9, v10
	v_cvt_pk_bf16_f32 v5, v11, v5
	global_store_dwordx4 v[18:19], v[2:5], off offset:256 sc1
	s_cbranch_vccnz .LBB0_926
	s_andn2_b64 vcc, exec, s[10:11]
	s_cbranch_vccnz .LBB0_903
	s_barrier
	s_branch .LBB0_903

.LBB0_1001:
	v_lshl_add_u32 v140, s44, 8, v142
	v_lshl_or_b32 v138, s45, 8, v143
	v_lshl_add_u32 v150, v140, 11, v138
	v_lshlrev_b32_e32 v150, 2, v150
	v_readlane_b32 s44, v254, 12
	v_readlane_b32 s45, v254, 13
	v_readlane_b32 s46, v254, 14
	v_readlane_b32 s47, v254, 15
	v_readlane_b32 s48, v254, 16
	v_readlane_b32 s49, v254, 17
	v_readlane_b32 s50, v254, 18
	v_readlane_b32 s51, v254, 19
	v_readlane_b32 s52, v254, 20
	v_readlane_b32 s53, v254, 21
	v_readlane_b32 s54, v254, 22
	v_readlane_b32 s55, v254, 23
	v_readlane_b32 s56, v254, 24
	v_readlane_b32 s57, v254, 25
	v_readlane_b32 s58, v254, 26
	v_readlane_b32 s59, v254, 27
	s_and_b64 vcc, exec, s[2:3]
	s_mov_b64 s[98:99], s[44:45]
	s_mov_b64 s[100:101], s[0:1]
	global_load_dwordx4 v[154:157], v150, s[98:99]
	global_load_dwordx4 v[158:161], v150, s[98:99] offset:64
	global_load_dwordx4 v[162:165], v150, s[98:99] offset:512
	global_load_dwordx4 v[166:169], v150, s[98:99] offset:576
	s_add_u32 s98, s98, 0x20000
	s_addc_u32 s99, s99, 0
	global_load_dwordx4 v[170:173], v150, s[98:99]
	global_load_dwordx4 v[174:177], v150, s[98:99] offset:64
	global_load_dwordx4 v[178:181], v150, s[98:99] offset:512
	global_load_dwordx4 v[182:185], v150, s[98:99] offset:576
	s_add_u32 s98, s98, 0x20000
	s_addc_u32 s99, s99, 0
	global_load_dwordx4 v[186:189], v150, s[98:99]
	global_load_dwordx4 v[190:193], v150, s[98:99] offset:64
	global_load_dwordx4 v[194:197], v150, s[98:99] offset:512
	global_load_dwordx4 v[198:201], v150, s[98:99] offset:576
	s_add_u32 s98, s98, 0x20000
	s_addc_u32 s99, s99, 0
	global_load_dwordx4 v[202:205], v150, s[98:99]
	global_load_dwordx4 v[206:209], v150, s[98:99] offset:64
	global_load_dwordx4 v[210:213], v150, s[98:99] offset:512
	global_load_dwordx4 v[214:217], v150, s[98:99] offset:576
	s_add_u32 s98, s98, 0xa0000
	s_addc_u32 s99, s99, 0
	s_waitcnt vmcnt(15)
	v_pk_add_f32 v[126:127], v[126:127], v[154:155]
	v_pk_add_f32 v[128:129], v[128:129], v[156:157]
	global_store_dwordx4 v150, v[126:129], s[100:101] sc1
	global_load_dwordx4 v[154:157], v150, s[98:99]
	s_waitcnt vmcnt(16)
	v_pk_add_f32 v[122:123], v[122:123], v[158:159]
	v_pk_add_f32 v[124:125], v[124:125], v[160:161]
	global_store_dwordx4 v150, v[122:125], s[100:101] offset:64 sc1
	global_load_dwordx4 v[158:161], v150, s[98:99] offset:64
	s_waitcnt vmcnt(17)
	v_pk_add_f32 v[118:119], v[118:119], v[162:163]
	v_pk_add_f32 v[120:121], v[120:121], v[164:165]
	global_store_dwordx4 v150, v[118:121], s[100:101] offset:512 sc1
	global_load_dwordx4 v[162:165], v150, s[98:99] offset:512
	s_waitcnt vmcnt(18)
	v_pk_add_f32 v[106:107], v[106:107], v[166:167]
	v_pk_add_f32 v[108:109], v[108:109], v[168:169]
	global_store_dwordx4 v150, v[106:109], s[100:101] offset:576 sc1
	s_add_u32 s100, s100, 0x20000
	s_addc_u32 s101, s101, 0
	global_load_dwordx4 v[166:169], v150, s[98:99] offset:576
	s_add_u32 s98, s98, 0x20000
	s_addc_u32 s99, s99, 0
	s_waitcnt vmcnt(19)
	v_pk_add_f32 v[114:115], v[114:115], v[170:171]
	v_pk_add_f32 v[116:117], v[116:117], v[172:173]
	global_store_dwordx4 v150, v[114:117], s[100:101] sc1
	global_load_dwordx4 v[170:173], v150, s[98:99]
	s_waitcnt vmcnt(20)
	v_pk_add_f32 v[110:111], v[110:111], v[174:175]
	v_pk_add_f32 v[112:113], v[112:113], v[176:177]
	global_store_dwordx4 v150, v[110:113], s[100:101] offset:64 sc1
	global_load_dwordx4 v[174:177], v150, s[98:99] offset:64
	s_waitcnt vmcnt(21)
	v_pk_add_f32 v[102:103], v[102:103], v[178:179]
	v_pk_add_f32 v[104:105], v[104:105], v[180:181]
	global_store_dwordx4 v150, v[102:105], s[100:101] offset:512 sc1
	global_load_dwordx4 v[178:181], v150, s[98:99] offset:512
	s_waitcnt vmcnt(22)
	v_pk_add_f32 v[90:91], v[90:91], v[182:183]
	v_pk_add_f32 v[92:93], v[92:93], v[184:185]
	global_store_dwordx4 v150, v[90:93], s[100:101] offset:576 sc1
	s_add_u32 s100, s100, 0x20000
	s_addc_u32 s101, s101, 0
	global_load_dwordx4 v[182:185], v150, s[98:99] offset:576
	s_add_u32 s98, s98, 0x20000
	s_addc_u32 s99, s99, 0
	s_waitcnt vmcnt(23)
	v_pk_add_f32 v[98:99], v[98:99], v[186:187]
	v_pk_add_f32 v[100:101], v[100:101], v[188:189]
	global_store_dwordx4 v150, v[98:101], s[100:101] sc1
	global_load_dwordx4 v[186:189], v150, s[98:99]
	s_waitcnt vmcnt(24)
	v_pk_add_f32 v[94:95], v[94:95], v[190:191]
	v_pk_add_f32 v[96:97], v[96:97], v[192:193]
	global_store_dwordx4 v150, v[94:97], s[100:101] offset:64 sc1
	global_load_dwordx4 v[190:193], v150, s[98:99] offset:64
	s_waitcnt vmcnt(25)
	v_pk_add_f32 v[86:87], v[86:87], v[194:195]
	v_pk_add_f32 v[88:89], v[88:89], v[196:197]
	global_store_dwordx4 v150, v[86:89], s[100:101] offset:512 sc1
	global_load_dwordx4 v[194:197], v150, s[98:99] offset:512
	s_waitcnt vmcnt(26)
	v_pk_add_f32 v[74:75], v[74:75], v[198:199]
	v_pk_add_f32 v[76:77], v[76:77], v[200:201]
	global_store_dwordx4 v150, v[74:77], s[100:101] offset:576 sc1
	s_add_u32 s100, s100, 0x20000
	s_addc_u32 s101, s101, 0
	global_load_dwordx4 v[198:201], v150, s[98:99] offset:576
	s_add_u32 s98, s98, 0x20000
	s_addc_u32 s99, s99, 0
	s_waitcnt vmcnt(27)
	v_pk_add_f32 v[82:83], v[82:83], v[202:203]
	v_pk_add_f32 v[84:85], v[84:85], v[204:205]
	global_store_dwordx4 v150, v[82:85], s[100:101] sc1
	global_load_dwordx4 v[202:205], v150, s[98:99]
	s_waitcnt vmcnt(28)
	v_pk_add_f32 v[78:79], v[78:79], v[206:207]
	v_pk_add_f32 v[80:81], v[80:81], v[208:209]
	global_store_dwordx4 v150, v[78:81], s[100:101] offset:64 sc1
	global_load_dwordx4 v[206:209], v150, s[98:99] offset:64
	s_waitcnt vmcnt(29)
	v_pk_add_f32 v[70:71], v[70:71], v[210:211]
	v_pk_add_f32 v[72:73], v[72:73], v[212:213]
	global_store_dwordx4 v150, v[70:73], s[100:101] offset:512 sc1
	global_load_dwordx4 v[210:213], v150, s[98:99] offset:512
	s_waitcnt vmcnt(30)
	v_pk_add_f32 v[66:67], v[66:67], v[214:215]
	v_pk_add_f32 v[68:69], v[68:69], v[216:217]
	global_store_dwordx4 v150, v[66:69], s[100:101] offset:576 sc1
	s_add_u32 s100, s100, 0xa0000
	s_addc_u32 s101, s101, 0
	global_load_dwordx4 v[214:217], v150, s[98:99] offset:576
	s_waitcnt vmcnt(30)
	v_pk_add_f32 v[62:63], v[62:63], v[154:155]
	v_pk_add_f32 v[64:65], v[64:65], v[156:157]
	global_store_dwordx4 v150, v[62:65], s[100:101] sc1
	s_waitcnt vmcnt(29)
	v_pk_add_f32 v[58:59], v[58:59], v[158:159]
	v_pk_add_f32 v[60:61], v[60:61], v[160:161]
	global_store_dwordx4 v150, v[58:61], s[100:101] offset:64 sc1
	s_waitcnt vmcnt(28)
	v_pk_add_f32 v[54:55], v[54:55], v[162:163]
	v_pk_add_f32 v[56:57], v[56:57], v[164:165]
	global_store_dwordx4 v150, v[54:57], s[100:101] offset:512 sc1
	s_waitcnt vmcnt(27)
	v_pk_add_f32 v[42:43], v[42:43], v[166:167]
	v_pk_add_f32 v[44:45], v[44:45], v[168:169]
	global_store_dwordx4 v150, v[42:45], s[100:101] offset:576 sc1
	s_add_u32 s100, s100, 0x20000
	s_addc_u32 s101, s101, 0
	s_waitcnt vmcnt(26)
	v_pk_add_f32 v[50:51], v[50:51], v[170:171]
	v_pk_add_f32 v[52:53], v[52:53], v[172:173]
	global_store_dwordx4 v150, v[50:53], s[100:101] sc1
	s_waitcnt vmcnt(25)
	v_pk_add_f32 v[46:47], v[46:47], v[174:175]
	v_pk_add_f32 v[48:49], v[48:49], v[176:177]
	global_store_dwordx4 v150, v[46:49], s[100:101] offset:64 sc1
	s_waitcnt vmcnt(24)
	v_pk_add_f32 v[38:39], v[38:39], v[178:179]
	v_pk_add_f32 v[40:41], v[40:41], v[180:181]
	global_store_dwordx4 v150, v[38:41], s[100:101] offset:512 sc1
	s_waitcnt vmcnt(23)
	v_pk_add_f32 v[26:27], v[26:27], v[182:183]
	v_pk_add_f32 v[28:29], v[28:29], v[184:185]
	global_store_dwordx4 v150, v[26:29], s[100:101] offset:576 sc1
	s_add_u32 s100, s100, 0x20000
	s_addc_u32 s101, s101, 0
	s_waitcnt vmcnt(22)
	v_pk_add_f32 v[34:35], v[34:35], v[186:187]
	v_pk_add_f32 v[36:37], v[36:37], v[188:189]
	global_store_dwordx4 v150, v[34:37], s[100:101] sc1
	s_waitcnt vmcnt(21)
	v_pk_add_f32 v[30:31], v[30:31], v[190:191]
	v_pk_add_f32 v[32:33], v[32:33], v[192:193]
	global_store_dwordx4 v150, v[30:33], s[100:101] offset:64 sc1
	s_waitcnt vmcnt(20)
	v_pk_add_f32 v[22:23], v[22:23], v[194:195]
	v_pk_add_f32 v[24:25], v[24:25], v[196:197]
	global_store_dwordx4 v150, v[22:25], s[100:101] offset:512 sc1
	s_waitcnt vmcnt(19)
	v_pk_add_f32 v[10:11], v[10:11], v[198:199]
	v_pk_add_f32 v[12:13], v[12:13], v[200:201]
	global_store_dwordx4 v150, v[10:13], s[100:101] offset:576 sc1
	s_add_u32 s100, s100, 0x20000
	s_addc_u32 s101, s101, 0
	s_waitcnt vmcnt(18)
	v_pk_add_f32 v[18:19], v[18:19], v[202:203]
	v_pk_add_f32 v[20:21], v[20:21], v[204:205]
	global_store_dwordx4 v150, v[18:21], s[100:101] sc1
	s_waitcnt vmcnt(17)
	v_pk_add_f32 v[14:15], v[14:15], v[206:207]
	v_pk_add_f32 v[16:17], v[16:17], v[208:209]
	global_store_dwordx4 v150, v[14:17], s[100:101] offset:64 sc1
	s_waitcnt vmcnt(16)
	v_pk_add_f32 v[6:7], v[6:7], v[210:211]
	v_pk_add_f32 v[8:9], v[8:9], v[212:213]
	global_store_dwordx4 v150, v[6:9], s[100:101] offset:512 sc1
	s_waitcnt vmcnt(15)
	v_pk_add_f32 v[2:3], v[2:3], v[214:215]
	v_pk_add_f32 v[4:5], v[4:5], v[216:217]
	global_store_dwordx4 v150, v[2:5], s[100:101] offset:576 sc1
	s_cbranch_vccnz .LBB0_1004
	s_andn2_b64 vcc, exec, s[10:11]
	s_cbranch_vccnz .LBB0_989
	s_barrier
	s_branch .LBB0_989

.LBB0_1591:
	s_waitcnt vmcnt(0)
	v_pk_add_f32 v[8:9], v[42:43], v[174:175]
	v_pk_add_f32 v[6:7], v[44:45], v[176:177]
	v_min_f32_e32 v8, 0x40e00000, v8
	v_min_f32_e32 v9, 0x40e00000, v9
	v_pk_mul_f32 v[10:11], v[8:9], s[20:21] op_sel_hi:[1,0]
	v_min_f32_e32 v6, 0x40e00000, v6
	v_exp_f32_e32 v10, v10
	v_exp_f32_e32 v11, v11
	v_min_f32_e32 v7, 0x40e00000, v7
	v_pk_mul_f32 v[16:17], v[6:7], s[20:21] op_sel_hi:[1,0]
	v_pk_add_f32 v[14:15], v[50:51], v[178:179]
	v_pk_add_f32 v[10:11], v[10:11], 1.0 op_sel_hi:[1,0]
	v_exp_f32_e32 v16, v16
	v_rcp_f32_e32 v10, v10
	v_rcp_f32_e32 v11, v11
	v_exp_f32_e32 v17, v17
	v_med3_f32 v14, v14, s53, v212
	v_med3_f32 v15, v15, s53, v212
	v_pk_mul_f32 v[8:9], v[8:9], v[10:11]
	v_pk_fma_f32 v[10:11], v[14:15], 4.0, 4.0 op_sel_hi:[1,0,0]
	v_pk_add_f32 v[14:15], v[16:17], 1.0 op_sel_hi:[1,0]
	v_pk_add_f32 v[12:13], v[52:53], v[180:181]
	v_rcp_f32_e32 v14, v14
	v_rcp_f32_e32 v15, v15
	v_pk_mul_f32 v[8:9], v[8:9], v[10:11]
	v_med3_f32 v10, v12, s53, v212
	v_med3_f32 v11, v13, s53, v212
	v_pk_add_f32 v[12:13], v[38:39], v[166:167]
	v_pk_mul_f32 v[6:7], v[6:7], v[14:15]
	v_min_f32_e32 v12, 0x40e00000, v12
	v_min_f32_e32 v13, 0x40e00000, v13
	v_pk_mul_f32 v[14:15], v[12:13], s[20:21] op_sel_hi:[1,0]
	v_pk_fma_f32 v[10:11], v[10:11], 4.0, 4.0 op_sel_hi:[1,0,0]
	v_exp_f32_e32 v14, v14
	v_exp_f32_e32 v15, v15
	v_pk_mul_f32 v[6:7], v[6:7], v[10:11]
	v_pk_add_f32 v[10:11], v[40:41], v[168:169]
	v_pk_add_f32 v[18:19], v[46:47], v[170:171]
	v_min_f32_e32 v10, 0x40e00000, v10
	v_min_f32_e32 v11, 0x40e00000, v11
	v_pk_add_f32 v[14:15], v[14:15], 1.0 op_sel_hi:[1,0]
	v_pk_mul_f32 v[20:21], v[10:11], s[20:21] op_sel_hi:[1,0]
	v_rcp_f32_e32 v14, v14
	v_rcp_f32_e32 v15, v15
	v_exp_f32_e32 v20, v20
	v_exp_f32_e32 v21, v21
	v_med3_f32 v18, v18, s53, v212
	v_med3_f32 v19, v19, s53, v212
	v_pk_mul_f32 v[12:13], v[12:13], v[14:15]
	v_pk_fma_f32 v[14:15], v[18:19], 4.0, 4.0 op_sel_hi:[1,0,0]
	v_pk_add_f32 v[18:19], v[20:21], 1.0 op_sel_hi:[1,0]
	v_pk_add_f32 v[16:17], v[48:49], v[172:173]
	v_rcp_f32_e32 v18, v18
	v_rcp_f32_e32 v19, v19
	v_pk_mul_f32 v[12:13], v[12:13], v[14:15]
	v_med3_f32 v15, v17, s53, v212
	v_mov_b32_e32 v17, v35
	v_med3_f32 v14, v16, s53, v212
	v_mov_b32_e32 v16, v35
	v_cvt_pk_fp8_f32 v17, v12, v13
	v_cvt_pk_fp8_f32 v16, v8, v9
	v_pk_mul_f32 v[10:11], v[10:11], v[18:19]
	v_pk_fma_f32 v[8:9], v[14:15], 4.0, 4.0 op_sel_hi:[1,0,0]
	v_lshl_add_u32 v4, s56, 8, v205
	v_pk_mul_f32 v[8:9], v[10:11], v[8:9]
	v_cvt_pk_fp8_f32 v16, v6, v7 op_sel:[0,0,1]
	v_cvt_pk_fp8_f32 v17, v8, v9 op_sel:[0,0,1]
	v_pk_add_f32 v[8:9], v[42:43], v[158:159]
	v_mov_b64_e32 v[2:3], s[0:1]
	v_min_f32_e32 v8, 0x40e00000, v8
	v_min_f32_e32 v9, 0x40e00000, v9
	v_pk_mul_f32 v[10:11], v[8:9], s[20:21] op_sel_hi:[1,0]
	v_mad_i64_i32 v[6:7], s[26:27], v4, s52, v[2:3]
	v_exp_f32_e32 v10, v10
	v_exp_f32_e32 v11, v11
	v_lshl_add_u64 v[6:7], v[6:7], 0, v[34:35]
	s_nop 15
	s_nop 15
	global_store_dwordx2 v[6:7], v[16:17], off sc1
	v_pk_add_f32 v[6:7], v[44:45], v[160:161]
	v_pk_add_f32 v[10:11], v[10:11], 1.0 op_sel_hi:[1,0]
	v_min_f32_e32 v6, 0x40e00000, v6
	v_min_f32_e32 v7, 0x40e00000, v7
	v_pk_mul_f32 v[16:17], v[6:7], s[20:21] op_sel_hi:[1,0]
	v_rcp_f32_e32 v10, v10
	v_rcp_f32_e32 v11, v11
	v_exp_f32_e32 v16, v16
	v_exp_f32_e32 v17, v17
	v_pk_add_f32 v[14:15], v[50:51], v[162:163]
	v_pk_mul_f32 v[8:9], v[8:9], v[10:11]
	v_med3_f32 v14, v14, s53, v212
	v_med3_f32 v15, v15, s53, v212
	v_pk_fma_f32 v[10:11], v[14:15], 4.0, 4.0 op_sel_hi:[1,0,0]
	v_pk_add_f32 v[14:15], v[16:17], 1.0 op_sel_hi:[1,0]
	v_pk_add_f32 v[12:13], v[52:53], v[164:165]
	v_rcp_f32_e32 v14, v14
	v_rcp_f32_e32 v15, v15
	v_pk_mul_f32 v[8:9], v[8:9], v[10:11]
	v_med3_f32 v10, v12, s53, v212
	v_med3_f32 v11, v13, s53, v212
	v_pk_add_f32 v[12:13], v[38:39], v[150:151]
	v_pk_mul_f32 v[6:7], v[6:7], v[14:15]
	v_min_f32_e32 v12, 0x40e00000, v12
	v_min_f32_e32 v13, 0x40e00000, v13
	v_pk_mul_f32 v[14:15], v[12:13], s[20:21] op_sel_hi:[1,0]
	v_pk_fma_f32 v[10:11], v[10:11], 4.0, 4.0 op_sel_hi:[1,0,0]
	v_exp_f32_e32 v14, v14
	v_exp_f32_e32 v15, v15
	v_pk_mul_f32 v[6:7], v[6:7], v[10:11]
	v_pk_add_f32 v[10:11], v[40:41], v[152:153]
	v_pk_add_f32 v[18:19], v[46:47], v[154:155]
	v_min_f32_e32 v10, 0x40e00000, v10
	v_min_f32_e32 v11, 0x40e00000, v11
	v_pk_add_f32 v[14:15], v[14:15], 1.0 op_sel_hi:[1,0]
	v_pk_mul_f32 v[20:21], v[10:11], s[20:21] op_sel_hi:[1,0]
	v_rcp_f32_e32 v14, v14
	v_rcp_f32_e32 v15, v15
	v_exp_f32_e32 v20, v20
	v_exp_f32_e32 v21, v21
	v_med3_f32 v18, v18, s53, v212
	v_med3_f32 v19, v19, s53, v212
	v_pk_mul_f32 v[12:13], v[12:13], v[14:15]
	v_pk_fma_f32 v[14:15], v[18:19], 4.0, 4.0 op_sel_hi:[1,0,0]
	v_pk_add_f32 v[18:19], v[20:21], 1.0 op_sel_hi:[1,0]
	v_pk_add_f32 v[16:17], v[48:49], v[156:157]
	v_rcp_f32_e32 v18, v18
	v_rcp_f32_e32 v19, v19
	v_pk_mul_f32 v[12:13], v[12:13], v[14:15]
	v_med3_f32 v15, v17, s53, v212
	v_mov_b32_e32 v17, v35
	v_med3_f32 v14, v16, s53, v212
	v_mov_b32_e32 v16, v35
	v_cvt_pk_fp8_f32 v17, v12, v13
	v_cvt_pk_fp8_f32 v16, v8, v9
	v_pk_mul_f32 v[10:11], v[10:11], v[18:19]
	v_pk_fma_f32 v[8:9], v[14:15], 4.0, 4.0 op_sel_hi:[1,0,0]
	v_or_b32_e32 v5, 16, v4
	v_pk_mul_f32 v[8:9], v[10:11], v[8:9]
	v_cvt_pk_fp8_f32 v16, v6, v7 op_sel:[0,0,1]
	v_cvt_pk_fp8_f32 v17, v8, v9 op_sel:[0,0,1]
	v_pk_add_f32 v[8:9], v[42:43], v[142:143]
	v_mad_i64_i32 v[6:7], s[26:27], v5, s52, v[2:3]
	v_min_f32_e32 v8, 0x40e00000, v8
	v_min_f32_e32 v9, 0x40e00000, v9
	v_pk_mul_f32 v[10:11], v[8:9], s[20:21] op_sel_hi:[1,0]
	v_lshl_add_u64 v[6:7], v[6:7], 0, v[34:35]
	v_exp_f32_e32 v10, v10
	v_exp_f32_e32 v11, v11
	global_store_dwordx2 v[6:7], v[16:17], off sc1
	v_pk_add_f32 v[6:7], v[44:45], v[144:145]
	v_pk_add_f32 v[14:15], v[50:51], v[146:147]
	v_min_f32_e32 v6, 0x40e00000, v6
	v_min_f32_e32 v7, 0x40e00000, v7
	v_pk_add_f32 v[10:11], v[10:11], 1.0 op_sel_hi:[1,0]
	v_pk_mul_f32 v[16:17], v[6:7], s[20:21] op_sel_hi:[1,0]
	v_rcp_f32_e32 v10, v10
	v_rcp_f32_e32 v11, v11
	v_exp_f32_e32 v16, v16
	v_exp_f32_e32 v17, v17
	v_med3_f32 v14, v14, s53, v212
	v_med3_f32 v15, v15, s53, v212
	v_pk_mul_f32 v[8:9], v[8:9], v[10:11]
	v_pk_fma_f32 v[10:11], v[14:15], 4.0, 4.0 op_sel_hi:[1,0,0]
	v_pk_add_f32 v[14:15], v[16:17], 1.0 op_sel_hi:[1,0]
	v_pk_add_f32 v[12:13], v[52:53], v[148:149]
	v_rcp_f32_e32 v14, v14
	v_rcp_f32_e32 v15, v15
	v_pk_mul_f32 v[8:9], v[8:9], v[10:11]
	v_med3_f32 v10, v12, s53, v212
	v_med3_f32 v11, v13, s53, v212
	v_pk_add_f32 v[12:13], v[38:39], v[134:135]
	v_pk_mul_f32 v[6:7], v[6:7], v[14:15]
	v_min_f32_e32 v12, 0x40e00000, v12
	v_min_f32_e32 v13, 0x40e00000, v13
	v_pk_mul_f32 v[14:15], v[12:13], s[20:21] op_sel_hi:[1,0]
	v_pk_fma_f32 v[10:11], v[10:11], 4.0, 4.0 op_sel_hi:[1,0,0]
	v_exp_f32_e32 v14, v14
	v_exp_f32_e32 v15, v15
	v_pk_mul_f32 v[6:7], v[6:7], v[10:11]
	v_pk_add_f32 v[10:11], v[40:41], v[136:137]
	v_pk_add_f32 v[18:19], v[46:47], v[138:139]
	v_min_f32_e32 v10, 0x40e00000, v10
	v_min_f32_e32 v11, 0x40e00000, v11
	v_pk_add_f32 v[14:15], v[14:15], 1.0 op_sel_hi:[1,0]
	v_pk_mul_f32 v[20:21], v[10:11], s[20:21] op_sel_hi:[1,0]
	v_rcp_f32_e32 v14, v14
	v_rcp_f32_e32 v15, v15
	v_exp_f32_e32 v20, v20
	v_exp_f32_e32 v21, v21
	v_med3_f32 v18, v18, s53, v212
	v_med3_f32 v19, v19, s53, v212
	v_pk_mul_f32 v[12:13], v[12:13], v[14:15]
	v_pk_fma_f32 v[14:15], v[18:19], 4.0, 4.0 op_sel_hi:[1,0,0]
	v_pk_add_f32 v[18:19], v[20:21], 1.0 op_sel_hi:[1,0]
	v_pk_add_f32 v[16:17], v[48:49], v[140:141]
	v_rcp_f32_e32 v18, v18
	v_rcp_f32_e32 v19, v19
	v_pk_mul_f32 v[12:13], v[12:13], v[14:15]
	v_med3_f32 v15, v17, s53, v212
	v_mov_b32_e32 v17, v35
	v_med3_f32 v14, v16, s53, v212
	v_mov_b32_e32 v16, v35
	v_cvt_pk_fp8_f32 v17, v12, v13
	v_cvt_pk_fp8_f32 v16, v8, v9
	v_pk_mul_f32 v[10:11], v[10:11], v[18:19]
	v_pk_fma_f32 v[8:9], v[14:15], 4.0, 4.0 op_sel_hi:[1,0,0]
	v_or_b32_e32 v5, 32, v4
	v_pk_mul_f32 v[8:9], v[10:11], v[8:9]
	v_cvt_pk_fp8_f32 v16, v6, v7 op_sel:[0,0,1]
	v_cvt_pk_fp8_f32 v17, v8, v9 op_sel:[0,0,1]
	v_pk_add_f32 v[8:9], v[42:43], v[126:127]
	v_mad_i64_i32 v[6:7], s[26:27], v5, s52, v[2:3]
	v_min_f32_e32 v8, 0x40e00000, v8
	v_min_f32_e32 v9, 0x40e00000, v9
	v_pk_mul_f32 v[10:11], v[8:9], s[20:21] op_sel_hi:[1,0]
	v_lshl_add_u64 v[6:7], v[6:7], 0, v[34:35]
	v_exp_f32_e32 v10, v10
	v_exp_f32_e32 v11, v11
	global_store_dwordx2 v[6:7], v[16:17], off sc1
	v_pk_add_f32 v[6:7], v[44:45], v[128:129]
	v_pk_add_f32 v[14:15], v[50:51], v[130:131]
	v_min_f32_e32 v6, 0x40e00000, v6
	v_min_f32_e32 v7, 0x40e00000, v7
	v_pk_add_f32 v[10:11], v[10:11], 1.0 op_sel_hi:[1,0]
	v_pk_mul_f32 v[16:17], v[6:7], s[20:21] op_sel_hi:[1,0]
	v_rcp_f32_e32 v10, v10
	v_rcp_f32_e32 v11, v11
	v_exp_f32_e32 v16, v16
	v_exp_f32_e32 v17, v17
	v_med3_f32 v14, v14, s53, v212
	v_med3_f32 v15, v15, s53, v212
	v_pk_mul_f32 v[8:9], v[8:9], v[10:11]
	v_pk_fma_f32 v[10:11], v[14:15], 4.0, 4.0 op_sel_hi:[1,0,0]
	v_pk_add_f32 v[14:15], v[16:17], 1.0 op_sel_hi:[1,0]
	v_pk_add_f32 v[12:13], v[52:53], v[132:133]
	v_rcp_f32_e32 v14, v14
	v_rcp_f32_e32 v15, v15
	v_pk_mul_f32 v[8:9], v[8:9], v[10:11]
	v_med3_f32 v10, v12, s53, v212
	v_med3_f32 v11, v13, s53, v212
	v_pk_add_f32 v[12:13], v[38:39], v[110:111]
	v_pk_mul_f32 v[6:7], v[6:7], v[14:15]
	v_min_f32_e32 v12, 0x40e00000, v12
	v_min_f32_e32 v13, 0x40e00000, v13
	v_pk_mul_f32 v[14:15], v[12:13], s[20:21] op_sel_hi:[1,0]
	v_pk_fma_f32 v[10:11], v[10:11], 4.0, 4.0 op_sel_hi:[1,0,0]
	v_exp_f32_e32 v14, v14
	v_exp_f32_e32 v15, v15
	v_pk_mul_f32 v[6:7], v[6:7], v[10:11]
	v_pk_add_f32 v[10:11], v[40:41], v[112:113]
	v_pk_add_f32 v[18:19], v[46:47], v[118:119]
	v_min_f32_e32 v10, 0x40e00000, v10
	v_min_f32_e32 v11, 0x40e00000, v11
	v_pk_add_f32 v[14:15], v[14:15], 1.0 op_sel_hi:[1,0]
	v_pk_mul_f32 v[20:21], v[10:11], s[20:21] op_sel_hi:[1,0]
	v_rcp_f32_e32 v14, v14
	v_rcp_f32_e32 v15, v15
	v_exp_f32_e32 v20, v20
	v_exp_f32_e32 v21, v21
	v_med3_f32 v18, v18, s53, v212
	v_med3_f32 v19, v19, s53, v212
	v_pk_mul_f32 v[12:13], v[12:13], v[14:15]
	v_pk_fma_f32 v[14:15], v[18:19], 4.0, 4.0 op_sel_hi:[1,0,0]
	v_pk_add_f32 v[18:19], v[20:21], 1.0 op_sel_hi:[1,0]
	v_pk_add_f32 v[16:17], v[48:49], v[120:121]
	v_rcp_f32_e32 v18, v18
	v_rcp_f32_e32 v19, v19
	v_pk_mul_f32 v[12:13], v[12:13], v[14:15]
	v_med3_f32 v15, v17, s53, v212
	v_mov_b32_e32 v17, v35
	v_med3_f32 v14, v16, s53, v212
	v_mov_b32_e32 v16, v35
	v_cvt_pk_fp8_f32 v17, v12, v13
	v_cvt_pk_fp8_f32 v16, v8, v9
	v_pk_mul_f32 v[10:11], v[10:11], v[18:19]
	v_pk_fma_f32 v[8:9], v[14:15], 4.0, 4.0 op_sel_hi:[1,0,0]
	v_or_b32_e32 v5, 48, v4
	v_pk_mul_f32 v[8:9], v[10:11], v[8:9]
	v_cvt_pk_fp8_f32 v16, v6, v7 op_sel:[0,0,1]
	v_cvt_pk_fp8_f32 v17, v8, v9 op_sel:[0,0,1]
	v_pk_add_f32 v[8:9], v[42:43], v[114:115]
	v_mad_i64_i32 v[6:7], s[26:27], v5, s52, v[2:3]
	v_min_f32_e32 v8, 0x40e00000, v8
	v_min_f32_e32 v9, 0x40e00000, v9
	v_pk_mul_f32 v[10:11], v[8:9], s[20:21] op_sel_hi:[1,0]
	v_lshl_add_u64 v[6:7], v[6:7], 0, v[34:35]
	v_exp_f32_e32 v10, v10
	v_exp_f32_e32 v11, v11
	global_store_dwordx2 v[6:7], v[16:17], off sc1
	v_pk_add_f32 v[6:7], v[44:45], v[116:117]
	v_pk_add_f32 v[14:15], v[50:51], v[122:123]
	v_min_f32_e32 v6, 0x40e00000, v6
	v_min_f32_e32 v7, 0x40e00000, v7
	v_pk_add_f32 v[10:11], v[10:11], 1.0 op_sel_hi:[1,0]
	v_pk_mul_f32 v[16:17], v[6:7], s[20:21] op_sel_hi:[1,0]
	v_rcp_f32_e32 v10, v10
	v_rcp_f32_e32 v11, v11
	v_exp_f32_e32 v16, v16
	v_exp_f32_e32 v17, v17
	v_med3_f32 v14, v14, s53, v212
	v_med3_f32 v15, v15, s53, v212
	v_pk_mul_f32 v[8:9], v[8:9], v[10:11]
	v_pk_fma_f32 v[10:11], v[14:15], 4.0, 4.0 op_sel_hi:[1,0,0]
	v_pk_add_f32 v[14:15], v[16:17], 1.0 op_sel_hi:[1,0]
	v_pk_add_f32 v[12:13], v[52:53], v[124:125]
	v_rcp_f32_e32 v14, v14
	v_rcp_f32_e32 v15, v15
	v_pk_mul_f32 v[8:9], v[8:9], v[10:11]
	v_med3_f32 v10, v12, s53, v212
	v_med3_f32 v11, v13, s53, v212
	v_pk_add_f32 v[12:13], v[38:39], v[102:103]
	v_pk_mul_f32 v[6:7], v[6:7], v[14:15]
	v_min_f32_e32 v12, 0x40e00000, v12
	v_min_f32_e32 v13, 0x40e00000, v13
	v_pk_mul_f32 v[14:15], v[12:13], s[20:21] op_sel_hi:[1,0]
	v_pk_fma_f32 v[10:11], v[10:11], 4.0, 4.0 op_sel_hi:[1,0,0]
	v_exp_f32_e32 v14, v14
	v_exp_f32_e32 v15, v15
	v_pk_mul_f32 v[6:7], v[6:7], v[10:11]
	v_pk_add_f32 v[10:11], v[40:41], v[104:105]
	v_pk_add_f32 v[18:19], v[46:47], v[106:107]
	v_min_f32_e32 v10, 0x40e00000, v10
	v_min_f32_e32 v11, 0x40e00000, v11
	v_pk_add_f32 v[14:15], v[14:15], 1.0 op_sel_hi:[1,0]
	v_pk_mul_f32 v[20:21], v[10:11], s[20:21] op_sel_hi:[1,0]
	v_rcp_f32_e32 v14, v14
	v_rcp_f32_e32 v15, v15
	v_exp_f32_e32 v20, v20
	v_exp_f32_e32 v21, v21
	v_med3_f32 v18, v18, s53, v212
	v_med3_f32 v19, v19, s53, v212
	v_pk_mul_f32 v[12:13], v[12:13], v[14:15]
	v_pk_fma_f32 v[14:15], v[18:19], 4.0, 4.0 op_sel_hi:[1,0,0]
	v_pk_add_f32 v[18:19], v[20:21], 1.0 op_sel_hi:[1,0]
	v_pk_add_f32 v[16:17], v[48:49], v[108:109]
	v_rcp_f32_e32 v18, v18
	v_rcp_f32_e32 v19, v19
	v_pk_mul_f32 v[12:13], v[12:13], v[14:15]
	v_med3_f32 v15, v17, s53, v212
	v_mov_b32_e32 v17, v35
	v_med3_f32 v14, v16, s53, v212
	v_mov_b32_e32 v16, v35
	v_cvt_pk_fp8_f32 v17, v12, v13
	v_cvt_pk_fp8_f32 v16, v8, v9
	v_pk_mul_f32 v[10:11], v[10:11], v[18:19]
	v_pk_fma_f32 v[8:9], v[14:15], 4.0, 4.0 op_sel_hi:[1,0,0]
	v_add_u32_e32 v5, 0x80, v4
	v_pk_mul_f32 v[8:9], v[10:11], v[8:9]
	v_cvt_pk_fp8_f32 v16, v6, v7 op_sel:[0,0,1]
	v_cvt_pk_fp8_f32 v17, v8, v9 op_sel:[0,0,1]
	v_pk_add_f32 v[8:9], v[42:43], v[94:95]
	v_mad_i64_i32 v[6:7], s[26:27], v5, s52, v[2:3]
	v_min_f32_e32 v8, 0x40e00000, v8
	v_min_f32_e32 v9, 0x40e00000, v9
	v_pk_mul_f32 v[10:11], v[8:9], s[20:21] op_sel_hi:[1,0]
	v_lshl_add_u64 v[6:7], v[6:7], 0, v[34:35]
	v_exp_f32_e32 v10, v10
	v_exp_f32_e32 v11, v11
	global_store_dwordx2 v[6:7], v[16:17], off sc1
	v_pk_add_f32 v[6:7], v[44:45], v[96:97]
	v_pk_add_f32 v[14:15], v[50:51], v[98:99]
	v_min_f32_e32 v6, 0x40e00000, v6
	v_min_f32_e32 v7, 0x40e00000, v7
	v_pk_add_f32 v[10:11], v[10:11], 1.0 op_sel_hi:[1,0]
	v_pk_mul_f32 v[16:17], v[6:7], s[20:21] op_sel_hi:[1,0]
	v_rcp_f32_e32 v10, v10
	v_rcp_f32_e32 v11, v11
	v_exp_f32_e32 v16, v16
	v_exp_f32_e32 v17, v17
	v_med3_f32 v14, v14, s53, v212
	v_med3_f32 v15, v15, s53, v212
	v_pk_mul_f32 v[8:9], v[8:9], v[10:11]
	v_pk_fma_f32 v[10:11], v[14:15], 4.0, 4.0 op_sel_hi:[1,0,0]
	v_pk_add_f32 v[14:15], v[16:17], 1.0 op_sel_hi:[1,0]
	v_pk_add_f32 v[12:13], v[52:53], v[100:101]
	v_rcp_f32_e32 v14, v14
	v_rcp_f32_e32 v15, v15
	v_pk_mul_f32 v[8:9], v[8:9], v[10:11]
	v_med3_f32 v10, v12, s53, v212
	v_med3_f32 v11, v13, s53, v212
	v_pk_add_f32 v[12:13], v[38:39], v[86:87]
	v_pk_mul_f32 v[6:7], v[6:7], v[14:15]
	v_min_f32_e32 v12, 0x40e00000, v12
	v_min_f32_e32 v13, 0x40e00000, v13
	v_pk_mul_f32 v[14:15], v[12:13], s[20:21] op_sel_hi:[1,0]
	v_pk_fma_f32 v[10:11], v[10:11], 4.0, 4.0 op_sel_hi:[1,0,0]
	v_exp_f32_e32 v14, v14
	v_exp_f32_e32 v15, v15
	v_pk_mul_f32 v[6:7], v[6:7], v[10:11]
	v_pk_add_f32 v[10:11], v[40:41], v[88:89]
	v_pk_add_f32 v[18:19], v[46:47], v[90:91]
	v_min_f32_e32 v10, 0x40e00000, v10
	v_min_f32_e32 v11, 0x40e00000, v11
	v_pk_add_f32 v[14:15], v[14:15], 1.0 op_sel_hi:[1,0]
	v_pk_mul_f32 v[20:21], v[10:11], s[20:21] op_sel_hi:[1,0]
	v_rcp_f32_e32 v14, v14
	v_rcp_f32_e32 v15, v15
	v_exp_f32_e32 v20, v20
	v_exp_f32_e32 v21, v21
	v_med3_f32 v18, v18, s53, v212
	v_med3_f32 v19, v19, s53, v212
	v_pk_mul_f32 v[12:13], v[12:13], v[14:15]
	v_pk_fma_f32 v[14:15], v[18:19], 4.0, 4.0 op_sel_hi:[1,0,0]
	v_pk_add_f32 v[18:19], v[20:21], 1.0 op_sel_hi:[1,0]
	v_pk_add_f32 v[16:17], v[48:49], v[92:93]
	v_rcp_f32_e32 v18, v18
	v_rcp_f32_e32 v19, v19
	v_pk_mul_f32 v[12:13], v[12:13], v[14:15]
	v_med3_f32 v15, v17, s53, v212
	v_mov_b32_e32 v17, v35
	v_med3_f32 v14, v16, s53, v212
	v_mov_b32_e32 v16, v35
	v_cvt_pk_fp8_f32 v17, v12, v13
	v_cvt_pk_fp8_f32 v16, v8, v9
	v_pk_mul_f32 v[10:11], v[10:11], v[18:19]
	v_pk_fma_f32 v[8:9], v[14:15], 4.0, 4.0 op_sel_hi:[1,0,0]
	v_add_u32_e32 v5, 0x90, v4
	v_pk_mul_f32 v[8:9], v[10:11], v[8:9]
	v_cvt_pk_fp8_f32 v16, v6, v7 op_sel:[0,0,1]
	v_cvt_pk_fp8_f32 v17, v8, v9 op_sel:[0,0,1]
	v_pk_add_f32 v[8:9], v[42:43], v[78:79]
	v_mad_i64_i32 v[6:7], s[26:27], v5, s52, v[2:3]
	v_min_f32_e32 v8, 0x40e00000, v8
	v_min_f32_e32 v9, 0x40e00000, v9
	v_pk_mul_f32 v[10:11], v[8:9], s[20:21] op_sel_hi:[1,0]
	v_lshl_add_u64 v[6:7], v[6:7], 0, v[34:35]
	v_exp_f32_e32 v10, v10
	v_exp_f32_e32 v11, v11
	global_store_dwordx2 v[6:7], v[16:17], off sc1
	v_pk_add_f32 v[6:7], v[44:45], v[80:81]
	v_pk_add_f32 v[14:15], v[50:51], v[82:83]
	v_min_f32_e32 v6, 0x40e00000, v6
	v_min_f32_e32 v7, 0x40e00000, v7
	v_pk_add_f32 v[10:11], v[10:11], 1.0 op_sel_hi:[1,0]
	v_pk_mul_f32 v[16:17], v[6:7], s[20:21] op_sel_hi:[1,0]
	v_rcp_f32_e32 v10, v10
	v_rcp_f32_e32 v11, v11
	v_exp_f32_e32 v16, v16
	v_exp_f32_e32 v17, v17
	v_med3_f32 v14, v14, s53, v212
	v_med3_f32 v15, v15, s53, v212
	v_pk_mul_f32 v[8:9], v[8:9], v[10:11]
	v_pk_fma_f32 v[10:11], v[14:15], 4.0, 4.0 op_sel_hi:[1,0,0]
	v_pk_add_f32 v[14:15], v[16:17], 1.0 op_sel_hi:[1,0]
	v_pk_add_f32 v[12:13], v[52:53], v[84:85]
	v_rcp_f32_e32 v14, v14
	v_rcp_f32_e32 v15, v15
	v_pk_mul_f32 v[8:9], v[8:9], v[10:11]
	v_med3_f32 v10, v12, s53, v212
	v_med3_f32 v11, v13, s53, v212
	v_pk_add_f32 v[12:13], v[38:39], v[70:71]
	v_pk_mul_f32 v[6:7], v[6:7], v[14:15]
	v_min_f32_e32 v12, 0x40e00000, v12
	v_min_f32_e32 v13, 0x40e00000, v13
	v_pk_mul_f32 v[14:15], v[12:13], s[20:21] op_sel_hi:[1,0]
	v_pk_fma_f32 v[10:11], v[10:11], 4.0, 4.0 op_sel_hi:[1,0,0]
	v_exp_f32_e32 v14, v14
	v_exp_f32_e32 v15, v15
	v_pk_mul_f32 v[6:7], v[6:7], v[10:11]
	v_pk_add_f32 v[10:11], v[40:41], v[72:73]
	v_pk_add_f32 v[18:19], v[46:47], v[74:75]
	v_min_f32_e32 v10, 0x40e00000, v10
	v_min_f32_e32 v11, 0x40e00000, v11
	v_pk_add_f32 v[14:15], v[14:15], 1.0 op_sel_hi:[1,0]
	v_pk_mul_f32 v[20:21], v[10:11], s[20:21] op_sel_hi:[1,0]
	v_rcp_f32_e32 v14, v14
	v_rcp_f32_e32 v15, v15
	v_exp_f32_e32 v20, v20
	v_exp_f32_e32 v21, v21
	v_med3_f32 v18, v18, s53, v212
	v_med3_f32 v19, v19, s53, v212
	v_pk_mul_f32 v[12:13], v[12:13], v[14:15]
	v_pk_fma_f32 v[14:15], v[18:19], 4.0, 4.0 op_sel_hi:[1,0,0]
	v_pk_add_f32 v[18:19], v[20:21], 1.0 op_sel_hi:[1,0]
	v_pk_add_f32 v[16:17], v[48:49], v[76:77]
	v_rcp_f32_e32 v18, v18
	v_rcp_f32_e32 v19, v19
	v_pk_mul_f32 v[12:13], v[12:13], v[14:15]
	v_med3_f32 v14, v16, s53, v212
	v_med3_f32 v15, v17, s53, v212
	v_mov_b32_e32 v16, v35
	v_mov_b32_e32 v17, v35
	v_cvt_pk_fp8_f32 v16, v8, v9
	v_cvt_pk_fp8_f32 v17, v12, v13
	v_pk_mul_f32 v[10:11], v[10:11], v[18:19]
	v_pk_fma_f32 v[8:9], v[14:15], 4.0, 4.0 op_sel_hi:[1,0,0]
	v_cvt_pk_fp8_f32 v16, v6, v7 op_sel:[0,0,1]
	v_pk_mul_f32 v[8:9], v[10:11], v[8:9]
	v_add_u32_e32 v5, 0xa0, v4
	v_cvt_pk_fp8_f32 v17, v8, v9 op_sel:[0,0,1]
	v_mad_i64_i32 v[6:7], s[26:27], v5, s52, v[2:3]
	v_lshl_add_u64 v[6:7], v[6:7], 0, v[34:35]
	global_store_dwordx2 v[6:7], v[16:17], off sc1
	v_pk_add_f32 v[6:7], v[42:43], v[66:67]
	v_add_u32_e32 v20, 0xb0, v4
	v_min_f32_e32 v6, 0x40e00000, v6
	v_min_f32_e32 v7, 0x40e00000, v7
	v_pk_mul_f32 v[8:9], v[6:7], s[20:21] op_sel_hi:[1,0]
	v_pk_add_f32 v[4:5], v[44:45], v[68:69]
	v_exp_f32_e32 v8, v8
	v_exp_f32_e32 v9, v9
	v_min_f32_e32 v4, 0x40e00000, v4
	v_min_f32_e32 v5, 0x40e00000, v5
	v_pk_mul_f32 v[14:15], v[4:5], s[20:21] op_sel_hi:[1,0]
	v_pk_add_f32 v[8:9], v[8:9], 1.0 op_sel_hi:[1,0]
	v_exp_f32_e32 v14, v14
	v_rcp_f32_e32 v8, v8
	v_rcp_f32_e32 v9, v9
	v_exp_f32_e32 v15, v15
	v_pk_add_f32 v[12:13], v[50:51], v[62:63]
	v_pk_add_f32 v[10:11], v[52:53], v[64:65]
	v_med3_f32 v12, v12, s53, v212
	v_med3_f32 v13, v13, s53, v212
	v_pk_mul_f32 v[6:7], v[6:7], v[8:9]
	v_pk_fma_f32 v[8:9], v[12:13], 4.0, 4.0 op_sel_hi:[1,0,0]
	v_pk_add_f32 v[12:13], v[14:15], 1.0 op_sel_hi:[1,0]
	v_pk_mul_f32 v[6:7], v[6:7], v[8:9]
	v_rcp_f32_e32 v12, v12
	v_rcp_f32_e32 v13, v13
	v_med3_f32 v8, v10, s53, v212
	v_med3_f32 v9, v11, s53, v212
	v_pk_add_f32 v[10:11], v[38:39], v[58:59]
	v_pk_mul_f32 v[4:5], v[4:5], v[12:13]
	v_min_f32_e32 v10, 0x40e00000, v10
	v_min_f32_e32 v11, 0x40e00000, v11
	v_pk_mul_f32 v[12:13], v[10:11], s[20:21] op_sel_hi:[1,0]
	v_pk_fma_f32 v[8:9], v[8:9], 4.0, 4.0 op_sel_hi:[1,0,0]
	v_exp_f32_e32 v12, v12
	v_exp_f32_e32 v13, v13
	v_pk_mul_f32 v[4:5], v[4:5], v[8:9]
	v_pk_add_f32 v[8:9], v[40:41], v[60:61]
	v_pk_add_f32 v[16:17], v[46:47], v[54:55]
	v_min_f32_e32 v8, 0x40e00000, v8
	v_min_f32_e32 v9, 0x40e00000, v9
	v_pk_add_f32 v[12:13], v[12:13], 1.0 op_sel_hi:[1,0]
	v_pk_mul_f32 v[18:19], v[8:9], s[20:21] op_sel_hi:[1,0]
	v_rcp_f32_e32 v12, v12
	v_rcp_f32_e32 v13, v13
	v_exp_f32_e32 v18, v18
	v_exp_f32_e32 v19, v19
	v_med3_f32 v16, v16, s53, v212
	v_med3_f32 v17, v17, s53, v212
	v_pk_mul_f32 v[10:11], v[10:11], v[12:13]
	v_pk_fma_f32 v[12:13], v[16:17], 4.0, 4.0 op_sel_hi:[1,0,0]
	v_pk_add_f32 v[16:17], v[18:19], 1.0 op_sel_hi:[1,0]
	v_pk_add_f32 v[14:15], v[48:49], v[56:57]
	v_rcp_f32_e32 v16, v16
	v_rcp_f32_e32 v17, v17
	v_pk_mul_f32 v[10:11], v[10:11], v[12:13]
	v_med3_f32 v12, v14, s53, v212
	v_med3_f32 v13, v15, s53, v212
	v_mov_b32_e32 v14, v35
	v_mov_b32_e32 v15, v35
	v_cvt_pk_fp8_f32 v14, v6, v7
	v_cvt_pk_fp8_f32 v15, v10, v11
	v_pk_mul_f32 v[8:9], v[8:9], v[16:17]
	v_pk_fma_f32 v[6:7], v[12:13], 4.0, 4.0 op_sel_hi:[1,0,0]
	v_cvt_pk_fp8_f32 v14, v4, v5 op_sel:[0,0,1]
	v_pk_mul_f32 v[6:7], v[8:9], v[6:7]
	v_mad_i64_i32 v[2:3], s[26:27], v20, s52, v[2:3]
	v_cvt_pk_fp8_f32 v15, v6, v7 op_sel:[0,0,1]
	v_lshl_add_u64 v[2:3], v[2:3], 0, v[34:35]
	s_and_b64 vcc, exec, s[2:3]
	global_store_dwordx2 v[2:3], v[14:15], off sc1
	s_cbranch_vccnz .LBB0_1594
	s_andn2_b64 vcc, exec, s[10:11]
	s_cbranch_vccnz .LBB0_1577
	s_barrier
	s_branch .LBB0_1577

.LBB0_1673:
	s_waitcnt vmcnt(0)
	v_pk_mul_f32 v[14:15], v[40:41], s[18:19] op_sel_hi:[1,0]
	v_lshl_add_u32 v18, s95, 8, v202
	v_pk_mul_f32 v[10:11], v[42:43], s[18:19] op_sel_hi:[1,0]
	v_ashrrev_i32_e32 v19, 31, v18
	v_pk_fma_f32 v[20:21], v[164:165], s[18:19], v[14:15] op_sel_hi:[1,0,1]
	v_pk_mul_f32 v[12:13], v[36:37], s[18:19] op_sel_hi:[1,0]
	v_lshlrev_b64 v[16:17], 11, v[18:19]
	v_med3_f32 v19, v20, s87, v209
	v_med3_f32 v23, v21, s87, v209
	v_pk_fma_f32 v[20:21], v[166:167], s[18:19], v[10:11] op_sel_hi:[1,0,1]
	v_mov_b32_e32 v22, v33
	v_med3_f32 v24, v20, s87, v209
	v_med3_f32 v25, v21, s87, v209
	v_pk_fma_f32 v[20:21], v[168:169], s[18:19], v[12:13] op_sel_hi:[1,0,1]
	v_cvt_pk_fp8_f32 v22, v19, v23
	v_med3_f32 v26, v20, s87, v209
	v_med3_f32 v27, v21, s87, v209
	v_mov_b32_e32 v23, v33
	v_cvt_pk_fp8_f32 v23, v26, v27
	v_pk_mul_f32 v[8:9], v[38:39], s[18:19] op_sel_hi:[1,0]
	v_pk_mul_f32 v[6:7], v[48:49], s[18:19] op_sel_hi:[1,0]
	v_pk_fma_f32 v[20:21], v[170:171], s[18:19], v[8:9] op_sel_hi:[1,0,1]
	v_pk_mul_f32 v[2:3], v[50:51], s[18:19] op_sel_hi:[1,0]
	v_med3_f32 v19, v20, s87, v209
	v_med3_f32 v20, v21, s87, v209
	v_cvt_pk_fp8_f32 v23, v19, v20 op_sel:[0,0,1]
	v_pk_fma_f32 v[20:21], v[172:173], s[18:19], v[6:7] op_sel_hi:[1,0,1]
	v_pk_mul_f32 v[4:5], v[44:45], s[18:19] op_sel_hi:[1,0]
	v_cvt_pk_fp8_f32 v22, v24, v25 op_sel:[0,0,1]
	v_med3_f32 v19, v20, s87, v209
	v_med3_f32 v25, v21, s87, v209
	v_pk_fma_f32 v[20:21], v[174:175], s[18:19], v[2:3] op_sel_hi:[1,0,1]
	v_mov_b32_e32 v24, v33
	v_med3_f32 v26, v20, s87, v209
	v_med3_f32 v27, v21, s87, v209
	v_pk_fma_f32 v[20:21], v[176:177], s[18:19], v[4:5] op_sel_hi:[1,0,1]
	v_cvt_pk_fp8_f32 v24, v19, v25
	v_med3_f32 v28, v20, s87, v209
	v_med3_f32 v29, v21, s87, v209
	v_mov_b32_e32 v25, v33
	v_cvt_pk_fp8_f32 v25, v28, v29
	v_pk_mul_f32 v[0:1], v[46:47], s[18:19] op_sel_hi:[1,0]
	v_cvt_pk_fp8_f32 v24, v26, v27 op_sel:[0,0,1]
	v_pk_fma_f32 v[20:21], v[178:179], s[18:19], v[0:1] op_sel_hi:[1,0,1]
	v_lshl_add_u64 v[16:17], s[4:5], 0, v[16:17]
	v_med3_f32 v19, v20, s87, v209
	v_med3_f32 v20, v21, s87, v209
	v_cvt_pk_fp8_f32 v25, v19, v20 op_sel:[0,0,1]
	v_lshl_add_u64 v[16:17], v[16:17], 0, v[32:33]
	s_nop 15
	s_nop 15
	global_store_dwordx2 v[16:17], v[22:23], off sc1
	global_store_dwordx2 v[16:17], v[24:25], off offset:128 sc1
	v_pk_fma_f32 v[22:23], v[152:153], s[18:19], v[14:15] op_sel_hi:[1,0,1]
	v_mov_b32_e32 v24, v33
	v_med3_f32 v19, v22, s87, v209
	v_med3_f32 v25, v23, s87, v209
	v_pk_fma_f32 v[22:23], v[154:155], s[18:19], v[10:11] op_sel_hi:[1,0,1]
	v_cvt_pk_fp8_f32 v24, v19, v25
	v_med3_f32 v26, v22, s87, v209
	v_med3_f32 v27, v23, s87, v209
	v_pk_fma_f32 v[22:23], v[148:149], s[18:19], v[12:13] op_sel_hi:[1,0,1]
	v_mov_b32_e32 v25, v33
	v_med3_f32 v28, v22, s87, v209
	v_med3_f32 v29, v23, s87, v209
	v_cvt_pk_fp8_f32 v25, v28, v29
	v_pk_fma_f32 v[22:23], v[150:151], s[18:19], v[8:9] op_sel_hi:[1,0,1]
	v_cvt_pk_fp8_f32 v24, v26, v27 op_sel:[0,0,1]
	v_med3_f32 v19, v22, s87, v209
	v_med3_f32 v22, v23, s87, v209
	v_cvt_pk_fp8_f32 v25, v19, v22 op_sel:[0,0,1]
	v_pk_fma_f32 v[22:23], v[160:161], s[18:19], v[6:7] op_sel_hi:[1,0,1]
	v_mov_b32_e32 v26, v33
	v_med3_f32 v19, v22, s87, v209
	v_med3_f32 v27, v23, s87, v209
	v_pk_fma_f32 v[22:23], v[162:163], s[18:19], v[2:3] op_sel_hi:[1,0,1]
	v_cvt_pk_fp8_f32 v26, v19, v27
	v_med3_f32 v28, v22, s87, v209
	v_med3_f32 v29, v23, s87, v209
	v_pk_fma_f32 v[22:23], v[156:157], s[18:19], v[4:5] op_sel_hi:[1,0,1]
	v_mov_b32_e32 v27, v33
	v_med3_f32 v30, v22, s87, v209
	v_med3_f32 v31, v23, s87, v209
	v_cvt_pk_fp8_f32 v27, v30, v31
	v_or_b32_e32 v20, 16, v18
	v_pk_fma_f32 v[22:23], v[158:159], s[18:19], v[0:1] op_sel_hi:[1,0,1]
	v_ashrrev_i32_e32 v21, 31, v20
	v_med3_f32 v19, v22, s87, v209
	v_med3_f32 v22, v23, s87, v209
	v_lshlrev_b64 v[20:21], 11, v[20:21]
	v_cvt_pk_fp8_f32 v26, v28, v29 op_sel:[0,0,1]
	v_cvt_pk_fp8_f32 v27, v19, v22 op_sel:[0,0,1]
	v_lshl_add_u64 v[20:21], s[4:5], 0, v[20:21]
	v_lshl_add_u64 v[20:21], v[20:21], 0, v[32:33]
	v_pk_fma_f32 v[22:23], v[136:137], s[18:19], v[14:15] op_sel_hi:[1,0,1]
	global_store_dwordx2 v[20:21], v[24:25], off sc1
	global_store_dwordx2 v[20:21], v[26:27], off offset:128 sc1
	v_med3_f32 v19, v22, s87, v209
	v_med3_f32 v25, v23, s87, v209
	v_pk_fma_f32 v[22:23], v[138:139], s[18:19], v[10:11] op_sel_hi:[1,0,1]
	v_mov_b32_e32 v24, v33
	v_med3_f32 v26, v22, s87, v209
	v_med3_f32 v27, v23, s87, v209
	v_pk_fma_f32 v[22:23], v[132:133], s[18:19], v[12:13] op_sel_hi:[1,0,1]
	v_cvt_pk_fp8_f32 v24, v19, v25
	v_med3_f32 v28, v22, s87, v209
	v_med3_f32 v29, v23, s87, v209
	v_mov_b32_e32 v25, v33
	v_cvt_pk_fp8_f32 v25, v28, v29
	v_pk_fma_f32 v[22:23], v[134:135], s[18:19], v[8:9] op_sel_hi:[1,0,1]
	v_cvt_pk_fp8_f32 v24, v26, v27 op_sel:[0,0,1]
	v_med3_f32 v19, v22, s87, v209
	v_med3_f32 v22, v23, s87, v209
	v_cvt_pk_fp8_f32 v25, v19, v22 op_sel:[0,0,1]
	v_pk_fma_f32 v[22:23], v[144:145], s[18:19], v[6:7] op_sel_hi:[1,0,1]
	v_mov_b32_e32 v26, v33
	v_med3_f32 v19, v22, s87, v209
	v_med3_f32 v27, v23, s87, v209
	v_pk_fma_f32 v[22:23], v[146:147], s[18:19], v[2:3] op_sel_hi:[1,0,1]
	v_cvt_pk_fp8_f32 v26, v19, v27
	v_med3_f32 v28, v22, s87, v209
	v_med3_f32 v29, v23, s87, v209
	v_pk_fma_f32 v[22:23], v[140:141], s[18:19], v[4:5] op_sel_hi:[1,0,1]
	v_mov_b32_e32 v27, v33
	v_med3_f32 v30, v22, s87, v209
	v_med3_f32 v31, v23, s87, v209
	v_cvt_pk_fp8_f32 v27, v30, v31
	v_or_b32_e32 v20, 32, v18
	v_pk_fma_f32 v[22:23], v[142:143], s[18:19], v[0:1] op_sel_hi:[1,0,1]
	v_ashrrev_i32_e32 v21, 31, v20
	v_med3_f32 v19, v22, s87, v209
	v_med3_f32 v22, v23, s87, v209
	v_lshlrev_b64 v[20:21], 11, v[20:21]
	v_cvt_pk_fp8_f32 v26, v28, v29 op_sel:[0,0,1]
	v_cvt_pk_fp8_f32 v27, v19, v22 op_sel:[0,0,1]
	v_lshl_add_u64 v[20:21], s[4:5], 0, v[20:21]
	v_lshl_add_u64 v[20:21], v[20:21], 0, v[32:33]
	global_store_dwordx2 v[20:21], v[24:25], off sc1
	global_store_dwordx2 v[20:21], v[26:27], off offset:128 sc1
	v_pk_fma_f32 v[20:21], v[112:113], s[18:19], v[14:15] op_sel_hi:[1,0,1]
	v_mov_b32_e32 v22, v33
	v_med3_f32 v23, v20, s87, v209
	v_med3_f32 v24, v21, s87, v209
	v_pk_fma_f32 v[20:21], v[114:115], s[18:19], v[10:11] op_sel_hi:[1,0,1]
	v_cvt_pk_fp8_f32 v22, v23, v24
	v_med3_f32 v25, v20, s87, v209
	v_med3_f32 v26, v21, s87, v209
	v_pk_fma_f32 v[20:21], v[104:105], s[18:19], v[12:13] op_sel_hi:[1,0,1]
	v_mov_b32_e32 v23, v33
	v_med3_f32 v27, v20, s87, v209
	v_med3_f32 v28, v21, s87, v209
	v_cvt_pk_fp8_f32 v23, v27, v28
	v_pk_fma_f32 v[20:21], v[106:107], s[18:19], v[8:9] op_sel_hi:[1,0,1]
	v_cvt_pk_fp8_f32 v22, v25, v26 op_sel:[0,0,1]
	v_med3_f32 v20, v20, s87, v209
	v_med3_f32 v21, v21, s87, v209
	v_cvt_pk_fp8_f32 v23, v20, v21 op_sel:[0,0,1]
	v_pk_fma_f32 v[20:21], v[108:109], s[18:19], v[6:7] op_sel_hi:[1,0,1]
	v_mov_b32_e32 v24, v33
	v_med3_f32 v25, v20, s87, v209
	v_med3_f32 v26, v21, s87, v209
	v_pk_fma_f32 v[20:21], v[110:111], s[18:19], v[2:3] op_sel_hi:[1,0,1]
	v_cvt_pk_fp8_f32 v24, v25, v26
	v_med3_f32 v27, v20, s87, v209
	v_med3_f32 v28, v21, s87, v209
	v_pk_fma_f32 v[20:21], v[100:101], s[18:19], v[4:5] op_sel_hi:[1,0,1]
	v_mov_b32_e32 v25, v33
	v_med3_f32 v29, v20, s87, v209
	v_med3_f32 v30, v21, s87, v209
	v_cvt_pk_fp8_f32 v25, v29, v30
	v_or_b32_e32 v18, 48, v18
	v_pk_fma_f32 v[20:21], v[102:103], s[18:19], v[0:1] op_sel_hi:[1,0,1]
	v_ashrrev_i32_e32 v19, 31, v18
	v_med3_f32 v20, v20, s87, v209
	v_med3_f32 v21, v21, s87, v209
	v_lshlrev_b64 v[18:19], 11, v[18:19]
	v_cvt_pk_fp8_f32 v24, v27, v28 op_sel:[0,0,1]
	v_cvt_pk_fp8_f32 v25, v20, v21 op_sel:[0,0,1]
	v_lshl_add_u64 v[18:19], s[4:5], 0, v[18:19]
	v_lshl_add_u64 v[18:19], v[18:19], 0, v[32:33]
	v_pk_fma_f32 v[20:21], v[124:125], s[18:19], v[14:15] op_sel_hi:[1,0,1]
	global_store_dwordx2 v[18:19], v[22:23], off sc1
	global_store_dwordx2 v[18:19], v[24:25], off offset:128 sc1
	v_med3_f32 v23, v20, s87, v209
	v_med3_f32 v24, v21, s87, v209
	v_pk_fma_f32 v[20:21], v[126:127], s[18:19], v[10:11] op_sel_hi:[1,0,1]
	v_mov_b32_e32 v22, v33
	v_med3_f32 v25, v20, s87, v209
	v_med3_f32 v26, v21, s87, v209
	v_pk_fma_f32 v[20:21], v[116:117], s[18:19], v[12:13] op_sel_hi:[1,0,1]
	v_cvt_pk_fp8_f32 v22, v23, v24
	v_med3_f32 v27, v20, s87, v209
	v_med3_f32 v28, v21, s87, v209
	v_mov_b32_e32 v23, v33
	v_cvt_pk_fp8_f32 v23, v27, v28
	v_pk_fma_f32 v[20:21], v[118:119], s[18:19], v[8:9] op_sel_hi:[1,0,1]
	v_cvt_pk_fp8_f32 v22, v25, v26 op_sel:[0,0,1]
	v_med3_f32 v20, v20, s87, v209
	v_med3_f32 v21, v21, s87, v209
	v_cvt_pk_fp8_f32 v23, v20, v21 op_sel:[0,0,1]
	v_pk_fma_f32 v[20:21], v[128:129], s[18:19], v[6:7] op_sel_hi:[1,0,1]
	v_mov_b32_e32 v24, v33
	v_med3_f32 v25, v20, s87, v209
	v_med3_f32 v26, v21, s87, v209
	v_pk_fma_f32 v[20:21], v[130:131], s[18:19], v[2:3] op_sel_hi:[1,0,1]
	v_cvt_pk_fp8_f32 v24, v25, v26
	v_med3_f32 v27, v20, s87, v209
	v_med3_f32 v28, v21, s87, v209
	v_pk_fma_f32 v[20:21], v[120:121], s[18:19], v[4:5] op_sel_hi:[1,0,1]
	v_mov_b32_e32 v25, v33
	v_med3_f32 v29, v20, s87, v209
	v_med3_f32 v30, v21, s87, v209
	v_cvt_pk_fp8_f32 v25, v29, v30
	v_pk_fma_f32 v[20:21], v[122:123], s[18:19], v[0:1] op_sel_hi:[1,0,1]
	v_cvt_pk_fp8_f32 v24, v27, v28 op_sel:[0,0,1]
	v_med3_f32 v20, v20, s87, v209
	v_med3_f32 v21, v21, s87, v209
	v_cvt_pk_fp8_f32 v25, v20, v21 op_sel:[0,0,1]
	v_add_co_u32_e32 v20, vcc, s88, v16
	v_lshl_add_u64 v[18:19], v[16:17], 0, s[20:21]
	s_nop 0
	v_addc_co_u32_e32 v21, vcc, 0, v17, vcc
	global_store_dwordx2 v[20:21], v[22:23], off sc1
	global_store_dwordx2 v[18:19], v[24:25], off offset:128 sc1
	v_pk_fma_f32 v[20:21], v[96:97], s[18:19], v[14:15] op_sel_hi:[1,0,1]
	v_mov_b32_e32 v22, v33
	v_med3_f32 v23, v20, s87, v209
	v_med3_f32 v24, v21, s87, v209
	v_pk_fma_f32 v[20:21], v[98:99], s[18:19], v[10:11] op_sel_hi:[1,0,1]
	v_cvt_pk_fp8_f32 v22, v23, v24
	v_med3_f32 v25, v20, s87, v209
	v_med3_f32 v26, v21, s87, v209
	v_pk_fma_f32 v[20:21], v[88:89], s[18:19], v[12:13] op_sel_hi:[1,0,1]
	v_mov_b32_e32 v23, v33
	v_med3_f32 v27, v20, s87, v209
	v_med3_f32 v28, v21, s87, v209
	v_cvt_pk_fp8_f32 v23, v27, v28
	v_pk_fma_f32 v[20:21], v[90:91], s[18:19], v[8:9] op_sel_hi:[1,0,1]
	v_cvt_pk_fp8_f32 v22, v25, v26 op_sel:[0,0,1]
	v_med3_f32 v20, v20, s87, v209
	v_med3_f32 v21, v21, s87, v209
	v_cvt_pk_fp8_f32 v23, v20, v21 op_sel:[0,0,1]
	v_pk_fma_f32 v[20:21], v[92:93], s[18:19], v[6:7] op_sel_hi:[1,0,1]
	v_mov_b32_e32 v24, v33
	v_med3_f32 v25, v20, s87, v209
	v_med3_f32 v26, v21, s87, v209
	v_pk_fma_f32 v[20:21], v[94:95], s[18:19], v[2:3] op_sel_hi:[1,0,1]
	v_cvt_pk_fp8_f32 v24, v25, v26
	v_med3_f32 v27, v20, s87, v209
	v_med3_f32 v28, v21, s87, v209
	v_pk_fma_f32 v[20:21], v[84:85], s[18:19], v[4:5] op_sel_hi:[1,0,1]
	v_mov_b32_e32 v25, v33
	v_med3_f32 v29, v20, s87, v209
	v_med3_f32 v30, v21, s87, v209
	v_cvt_pk_fp8_f32 v25, v29, v30
	v_pk_fma_f32 v[20:21], v[86:87], s[18:19], v[0:1] op_sel_hi:[1,0,1]
	v_cvt_pk_fp8_f32 v24, v27, v28 op_sel:[0,0,1]
	v_med3_f32 v20, v20, s87, v209
	v_med3_f32 v21, v21, s87, v209
	v_cvt_pk_fp8_f32 v25, v20, v21 op_sel:[0,0,1]
	v_add_co_u32_e32 v20, vcc, s89, v16
	v_lshl_add_u64 v[18:19], v[16:17], 0, s[22:23]
	s_nop 0
	v_addc_co_u32_e32 v21, vcc, 0, v17, vcc
	global_store_dwordx2 v[20:21], v[22:23], off sc1
	global_store_dwordx2 v[18:19], v[24:25], off offset:128 sc1
	v_pk_fma_f32 v[20:21], v[80:81], s[18:19], v[14:15] op_sel_hi:[1,0,1]
	v_mov_b32_e32 v22, v33
	v_med3_f32 v23, v20, s87, v209
	v_med3_f32 v24, v21, s87, v209
	v_pk_fma_f32 v[20:21], v[82:83], s[18:19], v[10:11] op_sel_hi:[1,0,1]
	v_cvt_pk_fp8_f32 v22, v23, v24
	v_med3_f32 v25, v20, s87, v209
	v_med3_f32 v26, v21, s87, v209
	v_pk_fma_f32 v[20:21], v[76:77], s[18:19], v[12:13] op_sel_hi:[1,0,1]
	v_mov_b32_e32 v23, v33
	v_med3_f32 v27, v20, s87, v209
	v_med3_f32 v28, v21, s87, v209
	v_cvt_pk_fp8_f32 v23, v27, v28
	v_pk_fma_f32 v[20:21], v[78:79], s[18:19], v[8:9] op_sel_hi:[1,0,1]
	v_cvt_pk_fp8_f32 v22, v25, v26 op_sel:[0,0,1]
	v_med3_f32 v20, v20, s87, v209
	v_med3_f32 v21, v21, s87, v209
	v_cvt_pk_fp8_f32 v23, v20, v21 op_sel:[0,0,1]
	v_pk_fma_f32 v[20:21], v[72:73], s[18:19], v[6:7] op_sel_hi:[1,0,1]
	v_mov_b32_e32 v24, v33
	v_med3_f32 v25, v20, s87, v209
	v_med3_f32 v26, v21, s87, v209
	v_pk_fma_f32 v[20:21], v[74:75], s[18:19], v[2:3] op_sel_hi:[1,0,1]
	v_cvt_pk_fp8_f32 v24, v25, v26
	v_med3_f32 v27, v20, s87, v209
	v_med3_f32 v28, v21, s87, v209
	v_pk_fma_f32 v[20:21], v[68:69], s[18:19], v[4:5] op_sel_hi:[1,0,1]
	v_mov_b32_e32 v25, v33
	v_med3_f32 v29, v20, s87, v209
	v_med3_f32 v30, v21, s87, v209
	v_cvt_pk_fp8_f32 v25, v29, v30
	v_pk_fma_f32 v[20:21], v[70:71], s[18:19], v[0:1] op_sel_hi:[1,0,1]
	v_cvt_pk_fp8_f32 v24, v27, v28 op_sel:[0,0,1]
	v_med3_f32 v20, v20, s87, v209
	v_med3_f32 v21, v21, s87, v209
	v_cvt_pk_fp8_f32 v25, v20, v21 op_sel:[0,0,1]
	v_add_co_u32_e32 v20, vcc, s90, v16
	v_pk_fma_f32 v[10:11], v[66:67], s[18:19], v[10:11] op_sel_hi:[1,0,1]
	s_nop 0
	v_addc_co_u32_e32 v21, vcc, 0, v17, vcc
	v_lshl_add_u64 v[18:19], v[16:17], 0, s[24:25]
	global_store_dwordx2 v[20:21], v[22:23], off sc1
	global_store_dwordx2 v[18:19], v[24:25], off offset:128 sc1
	v_med3_f32 v20, v10, s87, v209
	v_med3_f32 v21, v11, s87, v209
	v_pk_fma_f32 v[10:11], v[60:61], s[18:19], v[12:13] op_sel_hi:[1,0,1]
	v_pk_fma_f32 v[8:9], v[62:63], s[18:19], v[8:9] op_sel_hi:[1,0,1]
	v_med3_f32 v12, v10, s87, v209
	v_med3_f32 v13, v11, s87, v209
	v_mov_b32_e32 v11, v33
	v_cvt_pk_fp8_f32 v11, v12, v13
	v_med3_f32 v8, v8, s87, v209
	v_med3_f32 v9, v9, s87, v209
	v_pk_fma_f32 v[2:3], v[58:59], s[18:19], v[2:3] op_sel_hi:[1,0,1]
	v_pk_fma_f32 v[14:15], v[64:65], s[18:19], v[14:15] op_sel_hi:[1,0,1]
	v_cvt_pk_fp8_f32 v11, v8, v9 op_sel:[0,0,1]
	v_pk_fma_f32 v[6:7], v[56:57], s[18:19], v[6:7] op_sel_hi:[1,0,1]
	v_med3_f32 v8, v2, s87, v209
	v_med3_f32 v9, v3, s87, v209
	v_pk_fma_f32 v[2:3], v[52:53], s[18:19], v[4:5] op_sel_hi:[1,0,1]
	v_med3_f32 v14, v14, s87, v209
	v_med3_f32 v15, v15, s87, v209
	v_mov_b32_e32 v10, v33
	v_med3_f32 v6, v6, s87, v209
	v_med3_f32 v7, v7, s87, v209
	v_med3_f32 v4, v2, s87, v209
	v_med3_f32 v5, v3, s87, v209
	v_mov_b32_e32 v2, v33
	v_mov_b32_e32 v3, v33
	v_cvt_pk_fp8_f32 v10, v14, v15
	v_cvt_pk_fp8_f32 v2, v6, v7
	v_cvt_pk_fp8_f32 v3, v4, v5
	v_pk_fma_f32 v[0:1], v[54:55], s[18:19], v[0:1] op_sel_hi:[1,0,1]
	v_cvt_pk_fp8_f32 v10, v20, v21 op_sel:[0,0,1]
	v_med3_f32 v0, v0, s87, v209
	v_med3_f32 v1, v1, s87, v209
	v_cvt_pk_fp8_f32 v2, v8, v9 op_sel:[0,0,1]
	v_cvt_pk_fp8_f32 v3, v0, v1 op_sel:[0,0,1]
	v_add_co_u32_e32 v0, vcc, s91, v16
	v_readlane_b32 s82, v254, 53
	s_nop 0
	v_addc_co_u32_e32 v1, vcc, 0, v17, vcc
	v_lshl_add_u64 v[18:19], v[16:17], 0, s[26:27]
	s_and_b64 vcc, exec, s[2:3]
	s_mov_b32 s80, s78
	v_readlane_b32 s83, v254, 54
	global_store_dwordx2 v[0:1], v[10:11], off sc1
	global_store_dwordx2 v[18:19], v[2:3], off offset:128 sc1
	s_cbranch_vccnz .LBB0_1676
	s_andn2_b64 vcc, exec, s[10:11]
	s_cbranch_vccnz .LBB0_1659
	s_barrier
	s_branch .LBB0_1659
